# baseline (speedup 1.0000x reference)
.Lfunc_end6:
	.p2align	8
	.size	_Z6gemm_qILi0ELi1EEvPKDF16_S1_iiiiiiPKfS3_S3_S3_PDF16_8ConvArgs, .Lfunc_end6-_Z6gemm_qILi0ELi1EEvPKDF16_S1_iiiiiiPKfS3_S3_S3_PDF16_8ConvArgs
	.set _Z6gemm_qILi0ELi1EEvPKDF16_S1_iiiiiiPKfS3_S3_S3_PDF16_8ConvArgs.num_vgpr, 244
	.set _Z6gemm_qILi0ELi1EEvPKDF16_S1_iiiiiiPKfS3_S3_S3_PDF16_8ConvArgs.num_agpr, 0
	.set _Z6gemm_qILi0ELi1EEvPKDF16_S1_iiiiiiPKfS3_S3_S3_PDF16_8ConvArgs.numbered_sgpr, 44
	.set _Z6gemm_qILi0ELi1EEvPKDF16_S1_iiiiiiPKfS3_S3_S3_PDF16_8ConvArgs.num_named_barrier, 0
	.set _Z6gemm_qILi0ELi1EEvPKDF16_S1_iiiiiiPKfS3_S3_S3_PDF16_8ConvArgs.private_seg_size, 0
	.set _Z6gemm_qILi0ELi1EEvPKDF16_S1_iiiiiiPKfS3_S3_S3_PDF16_8ConvArgs.uses_vcc, 1
	.set _Z6gemm_qILi0ELi1EEvPKDF16_S1_iiiiiiPKfS3_S3_S3_PDF16_8ConvArgs.uses_flat_scratch, 0
	.set _Z6gemm_qILi0ELi1EEvPKDF16_S1_iiiiiiPKfS3_S3_S3_PDF16_8ConvArgs.has_dyn_sized_stack, 0
	.set _Z6gemm_qILi0ELi1EEvPKDF16_S1_iiiiiiPKfS3_S3_S3_PDF16_8ConvArgs.has_recursion, 0
	.set _Z6gemm_qILi0ELi1EEvPKDF16_S1_iiiiiiPKfS3_S3_S3_PDF16_8ConvArgs.has_indirect_call, 0

.Lfunc_end7:
	.p2align	8
	.size	_Z6gemm_pILi2ELi8EEvPKDF16_S1_iiiiiiPKfS3_S3_PfPDF16_S4_S5_S4_, .Lfunc_end7-_Z6gemm_pILi2ELi8EEvPKDF16_S1_iiiiiiPKfS3_S3_PfPDF16_S4_S5_S4_
	.set _Z6gemm_pILi2ELi8EEvPKDF16_S1_iiiiiiPKfS3_S3_PfPDF16_S4_S5_S4_.num_vgpr, 150
	.set _Z6gemm_pILi2ELi8EEvPKDF16_S1_iiiiiiPKfS3_S3_PfPDF16_S4_S5_S4_.num_agpr, 0
	.set _Z6gemm_pILi2ELi8EEvPKDF16_S1_iiiiiiPKfS3_S3_PfPDF16_S4_S5_S4_.numbered_sgpr, 35
	.set _Z6gemm_pILi2ELi8EEvPKDF16_S1_iiiiiiPKfS3_S3_PfPDF16_S4_S5_S4_.num_named_barrier, 0
	.set _Z6gemm_pILi2ELi8EEvPKDF16_S1_iiiiiiPKfS3_S3_PfPDF16_S4_S5_S4_.private_seg_size, 0
	.set _Z6gemm_pILi2ELi8EEvPKDF16_S1_iiiiiiPKfS3_S3_PfPDF16_S4_S5_S4_.uses_vcc, 1
	.set _Z6gemm_pILi2ELi8EEvPKDF16_S1_iiiiiiPKfS3_S3_PfPDF16_S4_S5_S4_.uses_flat_scratch, 0
	.set _Z6gemm_pILi2ELi8EEvPKDF16_S1_iiiiiiPKfS3_S3_PfPDF16_S4_S5_S4_.has_dyn_sized_stack, 0
	.set _Z6gemm_pILi2ELi8EEvPKDF16_S1_iiiiiiPKfS3_S3_PfPDF16_S4_S5_S4_.has_recursion, 0
	.set _Z6gemm_pILi2ELi8EEvPKDF16_S1_iiiiiiPKfS3_S3_PfPDF16_S4_S5_S4_.has_indirect_call, 0

.Lfunc_end8:
	.p2align	8
	.size	_Z6gemm_qILi1ELi0EEvPKDF16_S1_iiiiiiPKfS3_S3_S3_PDF16_8ConvArgs, .Lfunc_end8-_Z6gemm_qILi1ELi0EEvPKDF16_S1_iiiiiiPKfS3_S3_S3_PDF16_8ConvArgs
	.set _Z6gemm_qILi1ELi0EEvPKDF16_S1_iiiiiiPKfS3_S3_S3_PDF16_8ConvArgs.num_vgpr, 244
	.set _Z6gemm_qILi1ELi0EEvPKDF16_S1_iiiiiiPKfS3_S3_S3_PDF16_8ConvArgs.num_agpr, 0
	.set _Z6gemm_qILi1ELi0EEvPKDF16_S1_iiiiiiPKfS3_S3_S3_PDF16_8ConvArgs.numbered_sgpr, 23
	.set _Z6gemm_qILi1ELi0EEvPKDF16_S1_iiiiiiPKfS3_S3_S3_PDF16_8ConvArgs.num_named_barrier, 0
	.set _Z6gemm_qILi1ELi0EEvPKDF16_S1_iiiiiiPKfS3_S3_S3_PDF16_8ConvArgs.private_seg_size, 0
	.set _Z6gemm_qILi1ELi0EEvPKDF16_S1_iiiiiiPKfS3_S3_S3_PDF16_8ConvArgs.uses_vcc, 1
	.set _Z6gemm_qILi1ELi0EEvPKDF16_S1_iiiiiiPKfS3_S3_S3_PDF16_8ConvArgs.uses_flat_scratch, 0
	.set _Z6gemm_qILi1ELi0EEvPKDF16_S1_iiiiiiPKfS3_S3_S3_PDF16_8ConvArgs.has_dyn_sized_stack, 0
	.set _Z6gemm_qILi1ELi0EEvPKDF16_S1_iiiiiiPKfS3_S3_S3_PDF16_8ConvArgs.has_recursion, 0
	.set _Z6gemm_qILi1ELi0EEvPKDF16_S1_iiiiiiPKfS3_S3_S3_PDF16_8ConvArgs.has_indirect_call, 0

.LBB9_3:
	v_readfirstlane_b32 s44, v0
	v_add_u32_e32 v216, v79, v76
	v_add_u32_e32 v217, v79, v77
	v_add_u32_e32 v218, v80, v76
	v_add_u32_e32 v219, v80, v77
	s_lshl_b32 s44, s44, 4
	s_and_b32 s44, s44, 0xfffffc00
	v_add_u32_e32 v220, 0x10000, v216
	v_add_u32_e32 v221, 0x10000, v217
	v_add_u32_e32 v222, 0x10000, v218
	v_add_u32_e32 v223, 0x10000, v219
	s_movk_i32 s45, 0x180
	s_add_i32 m0, s44, 0x18000
	s_nop 0
	buffer_load_dwordx4 v72, s[4:7], s45 offen lds
	s_add_i32 m0, s44, 0x1a000
	s_nop 0
	buffer_load_dwordx4 v74, s[4:7], s45 offen lds
	s_add_i32 m0, s44, 0x1c000
	s_nop 0
	buffer_load_dwordx4 v73, s[12:15], s45 offen lds
	s_add_i32 m0, s44, 0x1e000
	s_nop 0
	buffer_load_dwordx4 v75, s[12:15], s45 offen lds
	s_waitcnt vmcnt(12)
	s_barrier
	ds_read_b128 v[152:155], v218 offset:16384
	ds_read_b128 v[156:159], v216
	ds_read_b128 v[160:163], v216 offset:4096
	ds_read_b128 v[164:167], v218 offset:20480
	ds_read_b128 v[168:171], v219 offset:16384
	ds_read_b128 v[172:175], v217
	ds_read_b128 v[176:179], v217 offset:4096
	ds_read_b128 v[180:183], v219 offset:20480
	s_waitcnt vmcnt(8) lgkmcnt(0)
	s_barrier
	s_movk_i32 s45, 0x200
	v_mfma_f32_32x32x16_f16 v[50:65], v[152:155], v[156:159], 0
	ds_read_b128 v[184:187], v218 offset:49152
	v_mfma_f32_32x32x16_f16 v[18:33], v[152:155], v[160:163], 0
	ds_read_b128 v[188:191], v216 offset:32768
	s_add_i32 m0, s44, 0x0
	s_nop 0
	buffer_load_dwordx4 v72, s[4:7], s45 offen lds
	v_mfma_f32_32x32x16_f16 v[34:49], v[164:167], v[156:159], 0
	ds_read_b128 v[192:195], v216 offset:36864
	s_add_i32 m0, s44, 0x2000
	s_nop 0
	buffer_load_dwordx4 v74, s[4:7], s45 offen lds
	v_mfma_f32_32x32x16_f16 v[2:17], v[164:167], v[160:163], 0
	ds_read_b128 v[196:199], v218 offset:53248
	s_add_i32 m0, s44, 0x4000
	s_nop 0
	buffer_load_dwordx4 v73, s[12:15], s45 offen lds
	v_mfma_f32_32x32x16_f16 v[50:65], v[168:171], v[172:175], v[50:65]
	ds_read_b128 v[200:203], v219 offset:49152
	s_add_i32 m0, s44, 0x6000
	s_nop 0
	buffer_load_dwordx4 v75, s[12:15], s45 offen lds
	v_mfma_f32_32x32x16_f16 v[18:33], v[168:171], v[176:179], v[18:33]
	ds_read_b128 v[204:207], v217 offset:32768
	v_mfma_f32_32x32x16_f16 v[34:49], v[180:183], v[172:175], v[34:49]
	ds_read_b128 v[208:211], v217 offset:36864
	v_mfma_f32_32x32x16_f16 v[2:17], v[180:183], v[176:179], v[2:17]
	ds_read_b128 v[212:215], v219 offset:53248
	s_waitcnt vmcnt(8) lgkmcnt(0)
	s_barrier
	s_movk_i32 s45, 0x280
	v_mfma_f32_32x32x16_f16 v[50:65], v[184:187], v[188:191], v[50:65]
	ds_read_b128 v[152:155], v222 offset:16384
	v_mfma_f32_32x32x16_f16 v[18:33], v[184:187], v[192:195], v[18:33]
	ds_read_b128 v[156:159], v220
	s_add_i32 m0, s44, 0x8000
	s_nop 0
	buffer_load_dwordx4 v72, s[4:7], s45 offen lds
	v_mfma_f32_32x32x16_f16 v[34:49], v[196:199], v[188:191], v[34:49]
	ds_read_b128 v[160:163], v220 offset:4096
	s_add_i32 m0, s44, 0xa000
	s_nop 0
	buffer_load_dwordx4 v74, s[4:7], s45 offen lds
	v_mfma_f32_32x32x16_f16 v[2:17], v[196:199], v[192:195], v[2:17]
	ds_read_b128 v[164:167], v222 offset:20480
	s_add_i32 m0, s44, 0xc000
	s_nop 0
	buffer_load_dwordx4 v73, s[12:15], s45 offen lds
	v_mfma_f32_32x32x16_f16 v[50:65], v[200:203], v[204:207], v[50:65]
	ds_read_b128 v[168:171], v223 offset:16384
	s_add_i32 m0, s44, 0xe000
	s_nop 0
	buffer_load_dwordx4 v75, s[12:15], s45 offen lds
	v_mfma_f32_32x32x16_f16 v[18:33], v[200:203], v[208:211], v[18:33]
	ds_read_b128 v[172:175], v221
	v_mfma_f32_32x32x16_f16 v[34:49], v[212:215], v[204:207], v[34:49]
	ds_read_b128 v[176:179], v221 offset:4096
	v_mfma_f32_32x32x16_f16 v[2:17], v[212:215], v[208:211], v[2:17]
	ds_read_b128 v[180:183], v223 offset:20480
	s_waitcnt vmcnt(8) lgkmcnt(0)
	s_barrier
	s_movk_i32 s45, 0x300
	v_mfma_f32_32x32x16_f16 v[50:65], v[152:155], v[156:159], v[50:65]
	ds_read_b128 v[184:187], v222 offset:49152
	v_mfma_f32_32x32x16_f16 v[18:33], v[152:155], v[160:163], v[18:33]
	ds_read_b128 v[188:191], v220 offset:32768
	s_add_i32 m0, s44, 0x10000
	s_nop 0
	buffer_load_dwordx4 v72, s[4:7], s45 offen lds
	v_mfma_f32_32x32x16_f16 v[34:49], v[164:167], v[156:159], v[34:49]
	ds_read_b128 v[192:195], v220 offset:36864
	s_add_i32 m0, s44, 0x12000
	s_nop 0
	buffer_load_dwordx4 v74, s[4:7], s45 offen lds
	v_mfma_f32_32x32x16_f16 v[2:17], v[164:167], v[160:163], v[2:17]
	ds_read_b128 v[196:199], v222 offset:53248
	s_add_i32 m0, s44, 0x14000
	s_nop 0
	buffer_load_dwordx4 v73, s[12:15], s45 offen lds
	v_mfma_f32_32x32x16_f16 v[50:65], v[168:171], v[172:175], v[50:65]
	ds_read_b128 v[200:203], v223 offset:49152
	s_add_i32 m0, s44, 0x16000
	s_nop 0
	buffer_load_dwordx4 v75, s[12:15], s45 offen lds
	v_mfma_f32_32x32x16_f16 v[18:33], v[168:171], v[176:179], v[18:33]
	ds_read_b128 v[204:207], v221 offset:32768
	v_mfma_f32_32x32x16_f16 v[34:49], v[180:183], v[172:175], v[34:49]
	ds_read_b128 v[208:211], v221 offset:36864
	v_mfma_f32_32x32x16_f16 v[2:17], v[180:183], v[176:179], v[2:17]
	ds_read_b128 v[212:215], v223 offset:53248
	s_waitcnt vmcnt(8) lgkmcnt(0)
	s_barrier
	s_movk_i32 s45, 0x380
	v_mfma_f32_32x32x16_f16 v[50:65], v[184:187], v[188:191], v[50:65]
	ds_read_b128 v[152:155], v218 offset:16384
	v_mfma_f32_32x32x16_f16 v[18:33], v[184:187], v[192:195], v[18:33]
	ds_read_b128 v[156:159], v216
	s_add_i32 m0, s44, 0x18000
	s_nop 0
	buffer_load_dwordx4 v72, s[4:7], s45 offen lds
	v_mfma_f32_32x32x16_f16 v[34:49], v[196:199], v[188:191], v[34:49]
	ds_read_b128 v[160:163], v216 offset:4096
	s_add_i32 m0, s44, 0x1a000
	s_nop 0
	buffer_load_dwordx4 v74, s[4:7], s45 offen lds
	v_mfma_f32_32x32x16_f16 v[2:17], v[196:199], v[192:195], v[2:17]
	ds_read_b128 v[164:167], v218 offset:20480
	s_add_i32 m0, s44, 0x1c000
	s_nop 0
	buffer_load_dwordx4 v73, s[12:15], s45 offen lds
	v_mfma_f32_32x32x16_f16 v[50:65], v[200:203], v[204:207], v[50:65]
	ds_read_b128 v[168:171], v219 offset:16384
	s_add_i32 m0, s44, 0x1e000
	s_nop 0
	buffer_load_dwordx4 v75, s[12:15], s45 offen lds
	v_mfma_f32_32x32x16_f16 v[18:33], v[200:203], v[208:211], v[18:33]
	ds_read_b128 v[172:175], v217
	v_mfma_f32_32x32x16_f16 v[34:49], v[212:215], v[204:207], v[34:49]
	ds_read_b128 v[176:179], v217 offset:4096
	v_mfma_f32_32x32x16_f16 v[2:17], v[212:215], v[208:211], v[2:17]
	ds_read_b128 v[180:183], v219 offset:20480
	s_waitcnt vmcnt(8) lgkmcnt(0)
	s_barrier
	s_movk_i32 s45, 0x400
	v_mfma_f32_32x32x16_f16 v[50:65], v[152:155], v[156:159], v[50:65]
	ds_read_b128 v[184:187], v218 offset:49152
	v_mfma_f32_32x32x16_f16 v[18:33], v[152:155], v[160:163], v[18:33]
	ds_read_b128 v[188:191], v216 offset:32768
	s_add_i32 m0, s44, 0x0
	s_nop 0
	buffer_load_dwordx4 v72, s[4:7], s45 offen lds
	v_mfma_f32_32x32x16_f16 v[34:49], v[164:167], v[156:159], v[34:49]
	ds_read_b128 v[192:195], v216 offset:36864
	s_add_i32 m0, s44, 0x2000
	s_nop 0
	buffer_load_dwordx4 v74, s[4:7], s45 offen lds
	v_mfma_f32_32x32x16_f16 v[2:17], v[164:167], v[160:163], v[2:17]
	ds_read_b128 v[196:199], v218 offset:53248
	s_add_i32 m0, s44, 0x4000
	s_nop 0
	buffer_load_dwordx4 v73, s[12:15], s45 offen lds
	v_mfma_f32_32x32x16_f16 v[50:65], v[168:171], v[172:175], v[50:65]
	ds_read_b128 v[200:203], v219 offset:49152
	s_add_i32 m0, s44, 0x6000
	s_nop 0
	buffer_load_dwordx4 v75, s[12:15], s45 offen lds
	v_mfma_f32_32x32x16_f16 v[18:33], v[168:171], v[176:179], v[18:33]
	ds_read_b128 v[204:207], v217 offset:32768
	v_mfma_f32_32x32x16_f16 v[34:49], v[180:183], v[172:175], v[34:49]
	ds_read_b128 v[208:211], v217 offset:36864
	v_mfma_f32_32x32x16_f16 v[2:17], v[180:183], v[176:179], v[2:17]
	ds_read_b128 v[212:215], v219 offset:53248
	s_waitcnt vmcnt(8) lgkmcnt(0)
	s_barrier
	s_movk_i32 s45, 0x480
	v_mfma_f32_32x32x16_f16 v[50:65], v[184:187], v[188:191], v[50:65]
	ds_read_b128 v[152:155], v222 offset:16384
	v_mfma_f32_32x32x16_f16 v[18:33], v[184:187], v[192:195], v[18:33]
	ds_read_b128 v[156:159], v220
	s_add_i32 m0, s44, 0x8000
	s_nop 0
	buffer_load_dwordx4 v72, s[4:7], s45 offen lds
	v_mfma_f32_32x32x16_f16 v[34:49], v[196:199], v[188:191], v[34:49]
	ds_read_b128 v[160:163], v220 offset:4096
	s_add_i32 m0, s44, 0xa000
	s_nop 0
	buffer_load_dwordx4 v74, s[4:7], s45 offen lds
	v_mfma_f32_32x32x16_f16 v[2:17], v[196:199], v[192:195], v[2:17]
	ds_read_b128 v[164:167], v222 offset:20480
	s_add_i32 m0, s44, 0xc000
	s_nop 0
	buffer_load_dwordx4 v73, s[12:15], s45 offen lds
	v_mfma_f32_32x32x16_f16 v[50:65], v[200:203], v[204:207], v[50:65]
	ds_read_b128 v[168:171], v223 offset:16384
	s_add_i32 m0, s44, 0xe000
	s_nop 0
	buffer_load_dwordx4 v75, s[12:15], s45 offen lds
	v_mfma_f32_32x32x16_f16 v[18:33], v[200:203], v[208:211], v[18:33]
	ds_read_b128 v[172:175], v221
	v_mfma_f32_32x32x16_f16 v[34:49], v[212:215], v[204:207], v[34:49]
	ds_read_b128 v[176:179], v221 offset:4096
	v_mfma_f32_32x32x16_f16 v[2:17], v[212:215], v[208:211], v[2:17]
	ds_read_b128 v[180:183], v223 offset:20480
	s_waitcnt vmcnt(8) lgkmcnt(0)
	s_barrier
	s_movk_i32 s45, 0x500
	v_mfma_f32_32x32x16_f16 v[50:65], v[152:155], v[156:159], v[50:65]
	ds_read_b128 v[184:187], v222 offset:49152
	v_mfma_f32_32x32x16_f16 v[18:33], v[152:155], v[160:163], v[18:33]
	ds_read_b128 v[188:191], v220 offset:32768
	s_add_i32 m0, s44, 0x10000
	s_nop 0
	buffer_load_dwordx4 v72, s[4:7], s45 offen lds
	v_mfma_f32_32x32x16_f16 v[34:49], v[164:167], v[156:159], v[34:49]
	ds_read_b128 v[192:195], v220 offset:36864
	s_add_i32 m0, s44, 0x12000
	s_nop 0
	buffer_load_dwordx4 v74, s[4:7], s45 offen lds
	v_mfma_f32_32x32x16_f16 v[2:17], v[164:167], v[160:163], v[2:17]
	ds_read_b128 v[196:199], v222 offset:53248
	s_add_i32 m0, s44, 0x14000
	s_nop 0
	buffer_load_dwordx4 v73, s[12:15], s45 offen lds
	v_mfma_f32_32x32x16_f16 v[50:65], v[168:171], v[172:175], v[50:65]
	ds_read_b128 v[200:203], v223 offset:49152
	s_add_i32 m0, s44, 0x16000
	s_nop 0
	buffer_load_dwordx4 v75, s[12:15], s45 offen lds
	v_mfma_f32_32x32x16_f16 v[18:33], v[168:171], v[176:179], v[18:33]
	ds_read_b128 v[204:207], v221 offset:32768
	v_mfma_f32_32x32x16_f16 v[34:49], v[180:183], v[172:175], v[34:49]
	ds_read_b128 v[208:211], v221 offset:36864
	v_mfma_f32_32x32x16_f16 v[2:17], v[180:183], v[176:179], v[2:17]
	ds_read_b128 v[212:215], v223 offset:53248
	s_waitcnt vmcnt(8) lgkmcnt(0)
	s_barrier
	s_movk_i32 s45, 0x580
	v_mfma_f32_32x32x16_f16 v[50:65], v[184:187], v[188:191], v[50:65]
	ds_read_b128 v[152:155], v218 offset:16384
	v_mfma_f32_32x32x16_f16 v[18:33], v[184:187], v[192:195], v[18:33]
	ds_read_b128 v[156:159], v216
	s_add_i32 m0, s44, 0x18000
	s_nop 0
	buffer_load_dwordx4 v72, s[4:7], s45 offen lds
	v_mfma_f32_32x32x16_f16 v[34:49], v[196:199], v[188:191], v[34:49]
	ds_read_b128 v[160:163], v216 offset:4096
	s_add_i32 m0, s44, 0x1a000
	s_nop 0
	buffer_load_dwordx4 v74, s[4:7], s45 offen lds
	v_mfma_f32_32x32x16_f16 v[2:17], v[196:199], v[192:195], v[2:17]
	ds_read_b128 v[164:167], v218 offset:20480
	s_add_i32 m0, s44, 0x1c000
	s_nop 0
	buffer_load_dwordx4 v73, s[12:15], s45 offen lds
	v_mfma_f32_32x32x16_f16 v[50:65], v[200:203], v[204:207], v[50:65]
	ds_read_b128 v[168:171], v219 offset:16384
	s_add_i32 m0, s44, 0x1e000
	s_nop 0
	buffer_load_dwordx4 v75, s[12:15], s45 offen lds
	v_mfma_f32_32x32x16_f16 v[18:33], v[200:203], v[208:211], v[18:33]
	ds_read_b128 v[172:175], v217
	v_mfma_f32_32x32x16_f16 v[34:49], v[212:215], v[204:207], v[34:49]
	ds_read_b128 v[176:179], v217 offset:4096
	v_mfma_f32_32x32x16_f16 v[2:17], v[212:215], v[208:211], v[2:17]
	ds_read_b128 v[180:183], v219 offset:20480
	s_waitcnt vmcnt(8) lgkmcnt(0)
	s_barrier
	s_movk_i32 s45, 0x600
	v_mfma_f32_32x32x16_f16 v[50:65], v[152:155], v[156:159], v[50:65]
	ds_read_b128 v[184:187], v218 offset:49152
	v_mfma_f32_32x32x16_f16 v[18:33], v[152:155], v[160:163], v[18:33]
	ds_read_b128 v[188:191], v216 offset:32768
	s_add_i32 m0, s44, 0x0
	s_nop 0
	buffer_load_dwordx4 v72, s[4:7], s45 offen lds
	v_mfma_f32_32x32x16_f16 v[34:49], v[164:167], v[156:159], v[34:49]
	ds_read_b128 v[192:195], v216 offset:36864
	s_add_i32 m0, s44, 0x2000
	s_nop 0
	buffer_load_dwordx4 v74, s[4:7], s45 offen lds
	v_mfma_f32_32x32x16_f16 v[2:17], v[164:167], v[160:163], v[2:17]
	ds_read_b128 v[196:199], v218 offset:53248
	s_add_i32 m0, s44, 0x4000
	s_nop 0
	buffer_load_dwordx4 v73, s[12:15], s45 offen lds
	v_mfma_f32_32x32x16_f16 v[50:65], v[168:171], v[172:175], v[50:65]
	ds_read_b128 v[200:203], v219 offset:49152
	s_add_i32 m0, s44, 0x6000
	s_nop 0
	buffer_load_dwordx4 v75, s[12:15], s45 offen lds
	v_mfma_f32_32x32x16_f16 v[18:33], v[168:171], v[176:179], v[18:33]
	ds_read_b128 v[204:207], v217 offset:32768
	v_mfma_f32_32x32x16_f16 v[34:49], v[180:183], v[172:175], v[34:49]
	ds_read_b128 v[208:211], v217 offset:36864
	v_mfma_f32_32x32x16_f16 v[2:17], v[180:183], v[176:179], v[2:17]
	ds_read_b128 v[212:215], v219 offset:53248
	s_waitcnt vmcnt(8) lgkmcnt(0)
	s_barrier
	s_movk_i32 s45, 0x680
	v_mfma_f32_32x32x16_f16 v[50:65], v[184:187], v[188:191], v[50:65]
	ds_read_b128 v[152:155], v222 offset:16384
	v_mfma_f32_32x32x16_f16 v[18:33], v[184:187], v[192:195], v[18:33]
	ds_read_b128 v[156:159], v220
	s_add_i32 m0, s44, 0x8000
	s_nop 0
	buffer_load_dwordx4 v72, s[4:7], s45 offen lds
	v_mfma_f32_32x32x16_f16 v[34:49], v[196:199], v[188:191], v[34:49]
	ds_read_b128 v[160:163], v220 offset:4096
	s_add_i32 m0, s44, 0xa000
	s_nop 0
	buffer_load_dwordx4 v74, s[4:7], s45 offen lds
	v_mfma_f32_32x32x16_f16 v[2:17], v[196:199], v[192:195], v[2:17]
	ds_read_b128 v[164:167], v222 offset:20480
	s_add_i32 m0, s44, 0xc000
	s_nop 0
	buffer_load_dwordx4 v73, s[12:15], s45 offen lds
	v_mfma_f32_32x32x16_f16 v[50:65], v[200:203], v[204:207], v[50:65]
	ds_read_b128 v[168:171], v223 offset:16384
	s_add_i32 m0, s44, 0xe000
	s_nop 0
	buffer_load_dwordx4 v75, s[12:15], s45 offen lds
	v_mfma_f32_32x32x16_f16 v[18:33], v[200:203], v[208:211], v[18:33]
	ds_read_b128 v[172:175], v221
	v_mfma_f32_32x32x16_f16 v[34:49], v[212:215], v[204:207], v[34:49]
	ds_read_b128 v[176:179], v221 offset:4096
	v_mfma_f32_32x32x16_f16 v[2:17], v[212:215], v[208:211], v[2:17]
	ds_read_b128 v[180:183], v223 offset:20480
	s_waitcnt vmcnt(8) lgkmcnt(0)
	s_barrier
	s_movk_i32 s45, 0x700
	v_mfma_f32_32x32x16_f16 v[50:65], v[152:155], v[156:159], v[50:65]
	ds_read_b128 v[184:187], v222 offset:49152
	v_mfma_f32_32x32x16_f16 v[18:33], v[152:155], v[160:163], v[18:33]
	ds_read_b128 v[188:191], v220 offset:32768
	s_add_i32 m0, s44, 0x10000
	s_nop 0
	buffer_load_dwordx4 v72, s[4:7], s45 offen lds
	v_mfma_f32_32x32x16_f16 v[34:49], v[164:167], v[156:159], v[34:49]
	ds_read_b128 v[192:195], v220 offset:36864
	s_add_i32 m0, s44, 0x12000
	s_nop 0
	buffer_load_dwordx4 v74, s[4:7], s45 offen lds
	v_mfma_f32_32x32x16_f16 v[2:17], v[164:167], v[160:163], v[2:17]
	ds_read_b128 v[196:199], v222 offset:53248
	s_add_i32 m0, s44, 0x14000
	s_nop 0
	buffer_load_dwordx4 v73, s[12:15], s45 offen lds
	v_mfma_f32_32x32x16_f16 v[50:65], v[168:171], v[172:175], v[50:65]
	ds_read_b128 v[200:203], v223 offset:49152
	s_add_i32 m0, s44, 0x16000
	s_nop 0
	buffer_load_dwordx4 v75, s[12:15], s45 offen lds
	v_mfma_f32_32x32x16_f16 v[18:33], v[168:171], v[176:179], v[18:33]
	ds_read_b128 v[204:207], v221 offset:32768
	v_mfma_f32_32x32x16_f16 v[34:49], v[180:183], v[172:175], v[34:49]
	ds_read_b128 v[208:211], v221 offset:36864
	v_mfma_f32_32x32x16_f16 v[2:17], v[180:183], v[176:179], v[2:17]
	ds_read_b128 v[212:215], v223 offset:53248
	s_waitcnt vmcnt(8) lgkmcnt(0)
	s_barrier
	s_movk_i32 s45, 0x780
	v_mfma_f32_32x32x16_f16 v[50:65], v[184:187], v[188:191], v[50:65]
	ds_read_b128 v[152:155], v218 offset:16384
	v_mfma_f32_32x32x16_f16 v[18:33], v[184:187], v[192:195], v[18:33]
	ds_read_b128 v[156:159], v216
	s_add_i32 m0, s44, 0x18000
	s_nop 0
	buffer_load_dwordx4 v72, s[4:7], s45 offen lds
	v_mfma_f32_32x32x16_f16 v[34:49], v[196:199], v[188:191], v[34:49]
	ds_read_b128 v[160:163], v216 offset:4096
	s_add_i32 m0, s44, 0x1a000
	s_nop 0
	buffer_load_dwordx4 v74, s[4:7], s45 offen lds
	v_mfma_f32_32x32x16_f16 v[2:17], v[196:199], v[192:195], v[2:17]
	ds_read_b128 v[164:167], v218 offset:20480
	s_add_i32 m0, s44, 0x1c000
	s_nop 0
	buffer_load_dwordx4 v73, s[12:15], s45 offen lds
	v_mfma_f32_32x32x16_f16 v[50:65], v[200:203], v[204:207], v[50:65]
	ds_read_b128 v[168:171], v219 offset:16384
	s_add_i32 m0, s44, 0x1e000
	s_nop 0
	buffer_load_dwordx4 v75, s[12:15], s45 offen lds
	v_mfma_f32_32x32x16_f16 v[18:33], v[200:203], v[208:211], v[18:33]
	ds_read_b128 v[172:175], v217
	v_mfma_f32_32x32x16_f16 v[34:49], v[212:215], v[204:207], v[34:49]
	ds_read_b128 v[176:179], v217 offset:4096
	v_mfma_f32_32x32x16_f16 v[2:17], v[212:215], v[208:211], v[2:17]
	ds_read_b128 v[180:183], v219 offset:20480
	s_waitcnt vmcnt(8) lgkmcnt(0)
	s_barrier
	s_movk_i32 s45, 0x800
	v_mfma_f32_32x32x16_f16 v[50:65], v[152:155], v[156:159], v[50:65]
	ds_read_b128 v[184:187], v218 offset:49152
	v_mfma_f32_32x32x16_f16 v[18:33], v[152:155], v[160:163], v[18:33]
	ds_read_b128 v[188:191], v216 offset:32768
	s_add_i32 m0, s44, 0x0
	s_nop 0
	buffer_load_dwordx4 v72, s[4:7], s45 offen lds
	v_mfma_f32_32x32x16_f16 v[34:49], v[164:167], v[156:159], v[34:49]
	ds_read_b128 v[192:195], v216 offset:36864
	s_add_i32 m0, s44, 0x2000
	s_nop 0
	buffer_load_dwordx4 v74, s[4:7], s45 offen lds
	v_mfma_f32_32x32x16_f16 v[2:17], v[164:167], v[160:163], v[2:17]
	ds_read_b128 v[196:199], v218 offset:53248
	s_add_i32 m0, s44, 0x4000
	s_nop 0
	buffer_load_dwordx4 v73, s[12:15], s45 offen lds
	v_mfma_f32_32x32x16_f16 v[50:65], v[168:171], v[172:175], v[50:65]
	ds_read_b128 v[200:203], v219 offset:49152
	s_add_i32 m0, s44, 0x6000
	s_nop 0
	buffer_load_dwordx4 v75, s[12:15], s45 offen lds
	v_mfma_f32_32x32x16_f16 v[18:33], v[168:171], v[176:179], v[18:33]
	ds_read_b128 v[204:207], v217 offset:32768
	v_mfma_f32_32x32x16_f16 v[34:49], v[180:183], v[172:175], v[34:49]
	ds_read_b128 v[208:211], v217 offset:36864
	v_mfma_f32_32x32x16_f16 v[2:17], v[180:183], v[176:179], v[2:17]
	ds_read_b128 v[212:215], v219 offset:53248
	s_waitcnt vmcnt(8) lgkmcnt(0)
	s_barrier
	s_movk_i32 s45, 0x880
	v_mfma_f32_32x32x16_f16 v[50:65], v[184:187], v[188:191], v[50:65]
	ds_read_b128 v[152:155], v222 offset:16384
	v_mfma_f32_32x32x16_f16 v[18:33], v[184:187], v[192:195], v[18:33]
	ds_read_b128 v[156:159], v220
	s_add_i32 m0, s44, 0x8000
	s_nop 0
	buffer_load_dwordx4 v72, s[4:7], s45 offen lds
	v_mfma_f32_32x32x16_f16 v[34:49], v[196:199], v[188:191], v[34:49]
	ds_read_b128 v[160:163], v220 offset:4096
	s_add_i32 m0, s44, 0xa000
	s_nop 0
	buffer_load_dwordx4 v74, s[4:7], s45 offen lds
	v_mfma_f32_32x32x16_f16 v[2:17], v[196:199], v[192:195], v[2:17]
	ds_read_b128 v[164:167], v222 offset:20480
	s_add_i32 m0, s44, 0xc000
	s_nop 0
	buffer_load_dwordx4 v73, s[12:15], s45 offen lds
	v_mfma_f32_32x32x16_f16 v[50:65], v[200:203], v[204:207], v[50:65]
	ds_read_b128 v[168:171], v223 offset:16384
	s_add_i32 m0, s44, 0xe000
	s_nop 0
	buffer_load_dwordx4 v75, s[12:15], s45 offen lds
	v_mfma_f32_32x32x16_f16 v[18:33], v[200:203], v[208:211], v[18:33]
	ds_read_b128 v[172:175], v221
	v_mfma_f32_32x32x16_f16 v[34:49], v[212:215], v[204:207], v[34:49]
	ds_read_b128 v[176:179], v221 offset:4096
	v_mfma_f32_32x32x16_f16 v[2:17], v[212:215], v[208:211], v[2:17]
	ds_read_b128 v[180:183], v223 offset:20480
	s_waitcnt vmcnt(8) lgkmcnt(0)
	s_barrier
	s_movk_i32 s45, 0x900
	v_mfma_f32_32x32x16_f16 v[50:65], v[152:155], v[156:159], v[50:65]
	ds_read_b128 v[184:187], v222 offset:49152
	v_mfma_f32_32x32x16_f16 v[18:33], v[152:155], v[160:163], v[18:33]
	ds_read_b128 v[188:191], v220 offset:32768
	s_add_i32 m0, s44, 0x10000
	s_nop 0
	buffer_load_dwordx4 v72, s[4:7], s45 offen lds
	v_mfma_f32_32x32x16_f16 v[34:49], v[164:167], v[156:159], v[34:49]
	ds_read_b128 v[192:195], v220 offset:36864
	s_add_i32 m0, s44, 0x12000
	s_nop 0
	buffer_load_dwordx4 v74, s[4:7], s45 offen lds
	v_mfma_f32_32x32x16_f16 v[2:17], v[164:167], v[160:163], v[2:17]
	ds_read_b128 v[196:199], v222 offset:53248
	s_add_i32 m0, s44, 0x14000
	s_nop 0
	buffer_load_dwordx4 v73, s[12:15], s45 offen lds
	v_mfma_f32_32x32x16_f16 v[50:65], v[168:171], v[172:175], v[50:65]
	ds_read_b128 v[200:203], v223 offset:49152
	s_add_i32 m0, s44, 0x16000
	s_nop 0
	buffer_load_dwordx4 v75, s[12:15], s45 offen lds
	v_mfma_f32_32x32x16_f16 v[18:33], v[168:171], v[176:179], v[18:33]
	ds_read_b128 v[204:207], v221 offset:32768
	v_mfma_f32_32x32x16_f16 v[34:49], v[180:183], v[172:175], v[34:49]
	ds_read_b128 v[208:211], v221 offset:36864
	v_mfma_f32_32x32x16_f16 v[2:17], v[180:183], v[176:179], v[2:17]
	ds_read_b128 v[212:215], v223 offset:53248
	s_waitcnt vmcnt(8) lgkmcnt(0)
	s_barrier
	s_movk_i32 s45, 0x980
	v_mfma_f32_32x32x16_f16 v[50:65], v[184:187], v[188:191], v[50:65]
	ds_read_b128 v[152:155], v218 offset:16384
	v_mfma_f32_32x32x16_f16 v[18:33], v[184:187], v[192:195], v[18:33]
	ds_read_b128 v[156:159], v216
	s_add_i32 m0, s44, 0x18000
	s_nop 0
	buffer_load_dwordx4 v72, s[4:7], s45 offen lds
	v_mfma_f32_32x32x16_f16 v[34:49], v[196:199], v[188:191], v[34:49]
	ds_read_b128 v[160:163], v216 offset:4096
	s_add_i32 m0, s44, 0x1a000
	s_nop 0
	buffer_load_dwordx4 v74, s[4:7], s45 offen lds
	v_mfma_f32_32x32x16_f16 v[2:17], v[196:199], v[192:195], v[2:17]
	ds_read_b128 v[164:167], v218 offset:20480
	s_add_i32 m0, s44, 0x1c000
	s_nop 0
	buffer_load_dwordx4 v73, s[12:15], s45 offen lds
	v_mfma_f32_32x32x16_f16 v[50:65], v[200:203], v[204:207], v[50:65]
	ds_read_b128 v[168:171], v219 offset:16384
	s_add_i32 m0, s44, 0x1e000
	s_nop 0
	buffer_load_dwordx4 v75, s[12:15], s45 offen lds
	v_mfma_f32_32x32x16_f16 v[18:33], v[200:203], v[208:211], v[18:33]
	ds_read_b128 v[172:175], v217
	v_mfma_f32_32x32x16_f16 v[34:49], v[212:215], v[204:207], v[34:49]
	ds_read_b128 v[176:179], v217 offset:4096
	v_mfma_f32_32x32x16_f16 v[2:17], v[212:215], v[208:211], v[2:17]
	ds_read_b128 v[180:183], v219 offset:20480
	s_waitcnt vmcnt(8) lgkmcnt(0)
	s_barrier
	s_movk_i32 s45, 0xa00
	v_mfma_f32_32x32x16_f16 v[50:65], v[152:155], v[156:159], v[50:65]
	ds_read_b128 v[184:187], v218 offset:49152
	v_mfma_f32_32x32x16_f16 v[18:33], v[152:155], v[160:163], v[18:33]
	ds_read_b128 v[188:191], v216 offset:32768
	s_add_i32 m0, s44, 0x0
	s_nop 0
	buffer_load_dwordx4 v72, s[4:7], s45 offen lds
	v_mfma_f32_32x32x16_f16 v[34:49], v[164:167], v[156:159], v[34:49]
	ds_read_b128 v[192:195], v216 offset:36864
	s_add_i32 m0, s44, 0x2000
	s_nop 0
	buffer_load_dwordx4 v74, s[4:7], s45 offen lds
	v_mfma_f32_32x32x16_f16 v[2:17], v[164:167], v[160:163], v[2:17]
	ds_read_b128 v[196:199], v218 offset:53248
	s_add_i32 m0, s44, 0x4000
	s_nop 0
	buffer_load_dwordx4 v73, s[12:15], s45 offen lds
	v_mfma_f32_32x32x16_f16 v[50:65], v[168:171], v[172:175], v[50:65]
	ds_read_b128 v[200:203], v219 offset:49152
	s_add_i32 m0, s44, 0x6000
	s_nop 0
	buffer_load_dwordx4 v75, s[12:15], s45 offen lds
	v_mfma_f32_32x32x16_f16 v[18:33], v[168:171], v[176:179], v[18:33]
	ds_read_b128 v[204:207], v217 offset:32768
	v_mfma_f32_32x32x16_f16 v[34:49], v[180:183], v[172:175], v[34:49]
	ds_read_b128 v[208:211], v217 offset:36864
	v_mfma_f32_32x32x16_f16 v[2:17], v[180:183], v[176:179], v[2:17]
	ds_read_b128 v[212:215], v219 offset:53248
	s_waitcnt vmcnt(8) lgkmcnt(0)
	s_barrier
	s_movk_i32 s45, 0xa80
	v_mfma_f32_32x32x16_f16 v[50:65], v[184:187], v[188:191], v[50:65]
	ds_read_b128 v[152:155], v222 offset:16384
	v_mfma_f32_32x32x16_f16 v[18:33], v[184:187], v[192:195], v[18:33]
	ds_read_b128 v[156:159], v220
	s_add_i32 m0, s44, 0x8000
	s_nop 0
	buffer_load_dwordx4 v72, s[4:7], s45 offen lds
	v_mfma_f32_32x32x16_f16 v[34:49], v[196:199], v[188:191], v[34:49]
	ds_read_b128 v[160:163], v220 offset:4096
	s_add_i32 m0, s44, 0xa000
	s_nop 0
	buffer_load_dwordx4 v74, s[4:7], s45 offen lds
	v_mfma_f32_32x32x16_f16 v[2:17], v[196:199], v[192:195], v[2:17]
	ds_read_b128 v[164:167], v222 offset:20480
	s_add_i32 m0, s44, 0xc000
	s_nop 0
	buffer_load_dwordx4 v73, s[12:15], s45 offen lds
	v_mfma_f32_32x32x16_f16 v[50:65], v[200:203], v[204:207], v[50:65]
	ds_read_b128 v[168:171], v223 offset:16384
	s_add_i32 m0, s44, 0xe000
	s_nop 0
	buffer_load_dwordx4 v75, s[12:15], s45 offen lds
	v_mfma_f32_32x32x16_f16 v[18:33], v[200:203], v[208:211], v[18:33]
	ds_read_b128 v[172:175], v221
	v_mfma_f32_32x32x16_f16 v[34:49], v[212:215], v[204:207], v[34:49]
	ds_read_b128 v[176:179], v221 offset:4096
	v_mfma_f32_32x32x16_f16 v[2:17], v[212:215], v[208:211], v[2:17]
	ds_read_b128 v[180:183], v223 offset:20480
	s_waitcnt vmcnt(8) lgkmcnt(0)
	s_barrier
	s_movk_i32 s45, 0xb00
	v_mfma_f32_32x32x16_f16 v[50:65], v[152:155], v[156:159], v[50:65]
	ds_read_b128 v[184:187], v222 offset:49152
	v_mfma_f32_32x32x16_f16 v[18:33], v[152:155], v[160:163], v[18:33]
	ds_read_b128 v[188:191], v220 offset:32768
	s_add_i32 m0, s44, 0x10000
	s_nop 0
	buffer_load_dwordx4 v72, s[4:7], s45 offen lds
	v_mfma_f32_32x32x16_f16 v[34:49], v[164:167], v[156:159], v[34:49]
	ds_read_b128 v[192:195], v220 offset:36864
	s_add_i32 m0, s44, 0x12000
	s_nop 0
	buffer_load_dwordx4 v74, s[4:7], s45 offen lds
	v_mfma_f32_32x32x16_f16 v[2:17], v[164:167], v[160:163], v[2:17]
	ds_read_b128 v[196:199], v222 offset:53248
	s_add_i32 m0, s44, 0x14000
	s_nop 0
	buffer_load_dwordx4 v73, s[12:15], s45 offen lds
	v_mfma_f32_32x32x16_f16 v[50:65], v[168:171], v[172:175], v[50:65]
	ds_read_b128 v[200:203], v223 offset:49152
	s_add_i32 m0, s44, 0x16000
	s_nop 0
	buffer_load_dwordx4 v75, s[12:15], s45 offen lds
	v_mfma_f32_32x32x16_f16 v[18:33], v[168:171], v[176:179], v[18:33]
	ds_read_b128 v[204:207], v221 offset:32768
	v_mfma_f32_32x32x16_f16 v[34:49], v[180:183], v[172:175], v[34:49]
	ds_read_b128 v[208:211], v221 offset:36864
	v_mfma_f32_32x32x16_f16 v[2:17], v[180:183], v[176:179], v[2:17]
	ds_read_b128 v[212:215], v223 offset:53248
	s_waitcnt vmcnt(8) lgkmcnt(0)
	s_barrier
	s_movk_i32 s45, 0xb80
	v_mfma_f32_32x32x16_f16 v[50:65], v[184:187], v[188:191], v[50:65]
	ds_read_b128 v[152:155], v218 offset:16384
	v_mfma_f32_32x32x16_f16 v[18:33], v[184:187], v[192:195], v[18:33]
	ds_read_b128 v[156:159], v216
	s_add_i32 m0, s44, 0x18000
	s_nop 0
	buffer_load_dwordx4 v72, s[4:7], s45 offen lds
	v_mfma_f32_32x32x16_f16 v[34:49], v[196:199], v[188:191], v[34:49]
	ds_read_b128 v[160:163], v216 offset:4096
	s_add_i32 m0, s44, 0x1a000
	s_nop 0
	buffer_load_dwordx4 v74, s[4:7], s45 offen lds
	v_mfma_f32_32x32x16_f16 v[2:17], v[196:199], v[192:195], v[2:17]
	ds_read_b128 v[164:167], v218 offset:20480
	s_add_i32 m0, s44, 0x1c000
	s_nop 0
	buffer_load_dwordx4 v73, s[12:15], s45 offen lds
	v_mfma_f32_32x32x16_f16 v[50:65], v[200:203], v[204:207], v[50:65]
	ds_read_b128 v[168:171], v219 offset:16384
	s_add_i32 m0, s44, 0x1e000
	s_nop 0
	buffer_load_dwordx4 v75, s[12:15], s45 offen lds
	v_mfma_f32_32x32x16_f16 v[18:33], v[200:203], v[208:211], v[18:33]
	ds_read_b128 v[172:175], v217
	v_mfma_f32_32x32x16_f16 v[34:49], v[212:215], v[204:207], v[34:49]
	ds_read_b128 v[176:179], v217 offset:4096
	v_mfma_f32_32x32x16_f16 v[2:17], v[212:215], v[208:211], v[2:17]
	ds_read_b128 v[180:183], v219 offset:20480
	s_waitcnt vmcnt(8) lgkmcnt(0)
	s_barrier
	s_movk_i32 s45, 0xc00
	v_mfma_f32_32x32x16_f16 v[50:65], v[152:155], v[156:159], v[50:65]
	ds_read_b128 v[184:187], v218 offset:49152
	v_mfma_f32_32x32x16_f16 v[18:33], v[152:155], v[160:163], v[18:33]
	ds_read_b128 v[188:191], v216 offset:32768
	s_add_i32 m0, s44, 0x0
	s_nop 0
	buffer_load_dwordx4 v72, s[4:7], s45 offen lds
	v_mfma_f32_32x32x16_f16 v[34:49], v[164:167], v[156:159], v[34:49]
	ds_read_b128 v[192:195], v216 offset:36864
	s_add_i32 m0, s44, 0x2000
	s_nop 0
	buffer_load_dwordx4 v74, s[4:7], s45 offen lds
	v_mfma_f32_32x32x16_f16 v[2:17], v[164:167], v[160:163], v[2:17]
	ds_read_b128 v[196:199], v218 offset:53248
	s_add_i32 m0, s44, 0x4000
	s_nop 0
	buffer_load_dwordx4 v73, s[12:15], s45 offen lds
	v_mfma_f32_32x32x16_f16 v[50:65], v[168:171], v[172:175], v[50:65]
	ds_read_b128 v[200:203], v219 offset:49152
	s_add_i32 m0, s44, 0x6000
	s_nop 0
	buffer_load_dwordx4 v75, s[12:15], s45 offen lds
	v_mfma_f32_32x32x16_f16 v[18:33], v[168:171], v[176:179], v[18:33]
	ds_read_b128 v[204:207], v217 offset:32768
	v_mfma_f32_32x32x16_f16 v[34:49], v[180:183], v[172:175], v[34:49]
	ds_read_b128 v[208:211], v217 offset:36864
	v_mfma_f32_32x32x16_f16 v[2:17], v[180:183], v[176:179], v[2:17]
	ds_read_b128 v[212:215], v219 offset:53248
	s_waitcnt vmcnt(8) lgkmcnt(0)
	s_barrier
	s_movk_i32 s45, 0xc80
	v_mfma_f32_32x32x16_f16 v[50:65], v[184:187], v[188:191], v[50:65]
	ds_read_b128 v[152:155], v222 offset:16384
	v_mfma_f32_32x32x16_f16 v[18:33], v[184:187], v[192:195], v[18:33]
	ds_read_b128 v[156:159], v220
	s_add_i32 m0, s44, 0x8000
	s_nop 0
	buffer_load_dwordx4 v72, s[4:7], s45 offen lds
	v_mfma_f32_32x32x16_f16 v[34:49], v[196:199], v[188:191], v[34:49]
	ds_read_b128 v[160:163], v220 offset:4096
	s_add_i32 m0, s44, 0xa000
	s_nop 0
	buffer_load_dwordx4 v74, s[4:7], s45 offen lds
	v_mfma_f32_32x32x16_f16 v[2:17], v[196:199], v[192:195], v[2:17]
	ds_read_b128 v[164:167], v222 offset:20480
	s_add_i32 m0, s44, 0xc000
	s_nop 0
	buffer_load_dwordx4 v73, s[12:15], s45 offen lds
	v_mfma_f32_32x32x16_f16 v[50:65], v[200:203], v[204:207], v[50:65]
	ds_read_b128 v[168:171], v223 offset:16384
	s_add_i32 m0, s44, 0xe000
	s_nop 0
	buffer_load_dwordx4 v75, s[12:15], s45 offen lds
	v_mfma_f32_32x32x16_f16 v[18:33], v[200:203], v[208:211], v[18:33]
	ds_read_b128 v[172:175], v221
	v_mfma_f32_32x32x16_f16 v[34:49], v[212:215], v[204:207], v[34:49]
	ds_read_b128 v[176:179], v221 offset:4096
	v_mfma_f32_32x32x16_f16 v[2:17], v[212:215], v[208:211], v[2:17]
	ds_read_b128 v[180:183], v223 offset:20480
	s_waitcnt vmcnt(8) lgkmcnt(0)
	s_barrier
	s_movk_i32 s45, 0xd00
	v_mfma_f32_32x32x16_f16 v[50:65], v[152:155], v[156:159], v[50:65]
	ds_read_b128 v[184:187], v222 offset:49152
	v_mfma_f32_32x32x16_f16 v[18:33], v[152:155], v[160:163], v[18:33]
	ds_read_b128 v[188:191], v220 offset:32768
	s_add_i32 m0, s44, 0x10000
	s_nop 0
	buffer_load_dwordx4 v72, s[4:7], s45 offen lds
	v_mfma_f32_32x32x16_f16 v[34:49], v[164:167], v[156:159], v[34:49]
	ds_read_b128 v[192:195], v220 offset:36864
	s_add_i32 m0, s44, 0x12000
	s_nop 0
	buffer_load_dwordx4 v74, s[4:7], s45 offen lds
	v_mfma_f32_32x32x16_f16 v[2:17], v[164:167], v[160:163], v[2:17]
	ds_read_b128 v[196:199], v222 offset:53248
	s_add_i32 m0, s44, 0x14000
	s_nop 0
	buffer_load_dwordx4 v73, s[12:15], s45 offen lds
	v_mfma_f32_32x32x16_f16 v[50:65], v[168:171], v[172:175], v[50:65]
	ds_read_b128 v[200:203], v223 offset:49152
	s_add_i32 m0, s44, 0x16000
	s_nop 0
	buffer_load_dwordx4 v75, s[12:15], s45 offen lds
	v_mfma_f32_32x32x16_f16 v[18:33], v[168:171], v[176:179], v[18:33]
	ds_read_b128 v[204:207], v221 offset:32768
	v_mfma_f32_32x32x16_f16 v[34:49], v[180:183], v[172:175], v[34:49]
	ds_read_b128 v[208:211], v221 offset:36864
	v_mfma_f32_32x32x16_f16 v[2:17], v[180:183], v[176:179], v[2:17]
	ds_read_b128 v[212:215], v223 offset:53248
	s_waitcnt vmcnt(8) lgkmcnt(0)
	s_barrier
	s_movk_i32 s45, 0xd80
	v_mfma_f32_32x32x16_f16 v[50:65], v[184:187], v[188:191], v[50:65]
	ds_read_b128 v[152:155], v218 offset:16384
	v_mfma_f32_32x32x16_f16 v[18:33], v[184:187], v[192:195], v[18:33]
	ds_read_b128 v[156:159], v216
	s_add_i32 m0, s44, 0x18000
	s_nop 0
	buffer_load_dwordx4 v72, s[4:7], s45 offen lds
	v_mfma_f32_32x32x16_f16 v[34:49], v[196:199], v[188:191], v[34:49]
	ds_read_b128 v[160:163], v216 offset:4096
	s_add_i32 m0, s44, 0x1a000
	s_nop 0
	buffer_load_dwordx4 v74, s[4:7], s45 offen lds
	v_mfma_f32_32x32x16_f16 v[2:17], v[196:199], v[192:195], v[2:17]
	ds_read_b128 v[164:167], v218 offset:20480
	s_add_i32 m0, s44, 0x1c000
	s_nop 0
	buffer_load_dwordx4 v73, s[12:15], s45 offen lds
	v_mfma_f32_32x32x16_f16 v[50:65], v[200:203], v[204:207], v[50:65]
	ds_read_b128 v[168:171], v219 offset:16384
	s_add_i32 m0, s44, 0x1e000
	s_nop 0
	buffer_load_dwordx4 v75, s[12:15], s45 offen lds
	v_mfma_f32_32x32x16_f16 v[18:33], v[200:203], v[208:211], v[18:33]
	ds_read_b128 v[172:175], v217
	v_mfma_f32_32x32x16_f16 v[34:49], v[212:215], v[204:207], v[34:49]
	ds_read_b128 v[176:179], v217 offset:4096
	v_mfma_f32_32x32x16_f16 v[2:17], v[212:215], v[208:211], v[2:17]
	ds_read_b128 v[180:183], v219 offset:20480
	s_waitcnt vmcnt(8) lgkmcnt(0)
	s_barrier
	s_movk_i32 s45, 0xe00
	v_mfma_f32_32x32x16_f16 v[50:65], v[152:155], v[156:159], v[50:65]
	ds_read_b128 v[184:187], v218 offset:49152
	v_mfma_f32_32x32x16_f16 v[18:33], v[152:155], v[160:163], v[18:33]
	ds_read_b128 v[188:191], v216 offset:32768
	s_add_i32 m0, s44, 0x0
	s_nop 0
	buffer_load_dwordx4 v72, s[4:7], s45 offen lds
	v_mfma_f32_32x32x16_f16 v[34:49], v[164:167], v[156:159], v[34:49]
	ds_read_b128 v[192:195], v216 offset:36864
	s_add_i32 m0, s44, 0x2000
	s_nop 0
	buffer_load_dwordx4 v74, s[4:7], s45 offen lds
	v_mfma_f32_32x32x16_f16 v[2:17], v[164:167], v[160:163], v[2:17]
	ds_read_b128 v[196:199], v218 offset:53248
	s_add_i32 m0, s44, 0x4000
	s_nop 0
	buffer_load_dwordx4 v73, s[12:15], s45 offen lds
	v_mfma_f32_32x32x16_f16 v[50:65], v[168:171], v[172:175], v[50:65]
	ds_read_b128 v[200:203], v219 offset:49152
	s_add_i32 m0, s44, 0x6000
	s_nop 0
	buffer_load_dwordx4 v75, s[12:15], s45 offen lds
	v_mfma_f32_32x32x16_f16 v[18:33], v[168:171], v[176:179], v[18:33]
	ds_read_b128 v[204:207], v217 offset:32768
	v_mfma_f32_32x32x16_f16 v[34:49], v[180:183], v[172:175], v[34:49]
	ds_read_b128 v[208:211], v217 offset:36864
	v_mfma_f32_32x32x16_f16 v[2:17], v[180:183], v[176:179], v[2:17]
	ds_read_b128 v[212:215], v219 offset:53248
	s_waitcnt vmcnt(8) lgkmcnt(0)
	s_barrier
	s_movk_i32 s45, 0xe80
	v_mfma_f32_32x32x16_f16 v[50:65], v[184:187], v[188:191], v[50:65]
	ds_read_b128 v[152:155], v222 offset:16384
	v_mfma_f32_32x32x16_f16 v[18:33], v[184:187], v[192:195], v[18:33]
	ds_read_b128 v[156:159], v220
	s_add_i32 m0, s44, 0x8000
	s_nop 0
	buffer_load_dwordx4 v72, s[4:7], s45 offen lds
	v_mfma_f32_32x32x16_f16 v[34:49], v[196:199], v[188:191], v[34:49]
	ds_read_b128 v[160:163], v220 offset:4096
	s_add_i32 m0, s44, 0xa000
	s_nop 0
	buffer_load_dwordx4 v74, s[4:7], s45 offen lds
	v_mfma_f32_32x32x16_f16 v[2:17], v[196:199], v[192:195], v[2:17]
	ds_read_b128 v[164:167], v222 offset:20480
	s_add_i32 m0, s44, 0xc000
	s_nop 0
	buffer_load_dwordx4 v73, s[12:15], s45 offen lds
	v_mfma_f32_32x32x16_f16 v[50:65], v[200:203], v[204:207], v[50:65]
	ds_read_b128 v[168:171], v223 offset:16384
	s_add_i32 m0, s44, 0xe000
	s_nop 0
	buffer_load_dwordx4 v75, s[12:15], s45 offen lds
	v_mfma_f32_32x32x16_f16 v[18:33], v[200:203], v[208:211], v[18:33]
	ds_read_b128 v[172:175], v221
	v_mfma_f32_32x32x16_f16 v[34:49], v[212:215], v[204:207], v[34:49]
	ds_read_b128 v[176:179], v221 offset:4096
	v_mfma_f32_32x32x16_f16 v[2:17], v[212:215], v[208:211], v[2:17]
	ds_read_b128 v[180:183], v223 offset:20480
	s_waitcnt vmcnt(8) lgkmcnt(0)
	s_barrier
	s_movk_i32 s45, 0xf00
	v_mfma_f32_32x32x16_f16 v[50:65], v[152:155], v[156:159], v[50:65]
	ds_read_b128 v[184:187], v222 offset:49152
	v_mfma_f32_32x32x16_f16 v[18:33], v[152:155], v[160:163], v[18:33]
	ds_read_b128 v[188:191], v220 offset:32768
	s_add_i32 m0, s44, 0x10000
	s_nop 0
	buffer_load_dwordx4 v72, s[4:7], s45 offen lds
	v_mfma_f32_32x32x16_f16 v[34:49], v[164:167], v[156:159], v[34:49]
	ds_read_b128 v[192:195], v220 offset:36864
	s_add_i32 m0, s44, 0x12000
	s_nop 0
	buffer_load_dwordx4 v74, s[4:7], s45 offen lds
	v_mfma_f32_32x32x16_f16 v[2:17], v[164:167], v[160:163], v[2:17]
	ds_read_b128 v[196:199], v222 offset:53248
	s_add_i32 m0, s44, 0x14000
	s_nop 0
	buffer_load_dwordx4 v73, s[12:15], s45 offen lds
	v_mfma_f32_32x32x16_f16 v[50:65], v[168:171], v[172:175], v[50:65]
	ds_read_b128 v[200:203], v223 offset:49152
	s_add_i32 m0, s44, 0x16000
	s_nop 0
	buffer_load_dwordx4 v75, s[12:15], s45 offen lds
	v_mfma_f32_32x32x16_f16 v[18:33], v[168:171], v[176:179], v[18:33]
	ds_read_b128 v[204:207], v221 offset:32768
	v_mfma_f32_32x32x16_f16 v[34:49], v[180:183], v[172:175], v[34:49]
	ds_read_b128 v[208:211], v221 offset:36864
	v_mfma_f32_32x32x16_f16 v[2:17], v[180:183], v[176:179], v[2:17]
	ds_read_b128 v[212:215], v223 offset:53248
	s_waitcnt vmcnt(8) lgkmcnt(0)
	s_barrier
	s_movk_i32 s45, 0xf80
	v_mfma_f32_32x32x16_f16 v[50:65], v[184:187], v[188:191], v[50:65]
	ds_read_b128 v[152:155], v218 offset:16384
	v_mfma_f32_32x32x16_f16 v[18:33], v[184:187], v[192:195], v[18:33]
	ds_read_b128 v[156:159], v216
	s_add_i32 m0, s44, 0x18000
	s_nop 0
	buffer_load_dwordx4 v72, s[4:7], s45 offen lds
	v_mfma_f32_32x32x16_f16 v[34:49], v[196:199], v[188:191], v[34:49]
	ds_read_b128 v[160:163], v216 offset:4096
	s_add_i32 m0, s44, 0x1a000
	s_nop 0
	buffer_load_dwordx4 v74, s[4:7], s45 offen lds
	v_mfma_f32_32x32x16_f16 v[2:17], v[196:199], v[192:195], v[2:17]
	ds_read_b128 v[164:167], v218 offset:20480
	s_add_i32 m0, s44, 0x1c000
	s_nop 0
	buffer_load_dwordx4 v73, s[12:15], s45 offen lds
	v_mfma_f32_32x32x16_f16 v[50:65], v[200:203], v[204:207], v[50:65]
	ds_read_b128 v[168:171], v219 offset:16384
	s_add_i32 m0, s44, 0x1e000
	s_nop 0
	buffer_load_dwordx4 v75, s[12:15], s45 offen lds
	v_mfma_f32_32x32x16_f16 v[18:33], v[200:203], v[208:211], v[18:33]
	ds_read_b128 v[172:175], v217
	v_mfma_f32_32x32x16_f16 v[34:49], v[212:215], v[204:207], v[34:49]
	ds_read_b128 v[176:179], v217 offset:4096
	v_mfma_f32_32x32x16_f16 v[2:17], v[212:215], v[208:211], v[2:17]
	ds_read_b128 v[180:183], v219 offset:20480
	s_waitcnt vmcnt(8) lgkmcnt(0)
	s_barrier
	v_mfma_f32_32x32x16_f16 v[50:65], v[152:155], v[156:159], v[50:65]
	ds_read_b128 v[184:187], v218 offset:49152
	v_mfma_f32_32x32x16_f16 v[18:33], v[152:155], v[160:163], v[18:33]
	ds_read_b128 v[188:191], v216 offset:32768
	v_mfma_f32_32x32x16_f16 v[34:49], v[164:167], v[156:159], v[34:49]
	ds_read_b128 v[192:195], v216 offset:36864
	v_mfma_f32_32x32x16_f16 v[2:17], v[164:167], v[160:163], v[2:17]
	ds_read_b128 v[196:199], v218 offset:53248
	v_mfma_f32_32x32x16_f16 v[50:65], v[168:171], v[172:175], v[50:65]
	ds_read_b128 v[200:203], v219 offset:49152
	v_mfma_f32_32x32x16_f16 v[18:33], v[168:171], v[176:179], v[18:33]
	ds_read_b128 v[204:207], v217 offset:32768
	v_mfma_f32_32x32x16_f16 v[34:49], v[180:183], v[172:175], v[34:49]
	ds_read_b128 v[208:211], v217 offset:36864
	v_mfma_f32_32x32x16_f16 v[2:17], v[180:183], v[176:179], v[2:17]
	ds_read_b128 v[212:215], v219 offset:53248
	s_waitcnt vmcnt(4) lgkmcnt(0)
	s_barrier
	v_mfma_f32_32x32x16_f16 v[50:65], v[184:187], v[188:191], v[50:65]
	ds_read_b128 v[152:155], v222 offset:16384
	v_mfma_f32_32x32x16_f16 v[18:33], v[184:187], v[192:195], v[18:33]
	ds_read_b128 v[156:159], v220
	v_mfma_f32_32x32x16_f16 v[34:49], v[196:199], v[188:191], v[34:49]
	ds_read_b128 v[160:163], v220 offset:4096
	v_mfma_f32_32x32x16_f16 v[2:17], v[196:199], v[192:195], v[2:17]
	ds_read_b128 v[164:167], v222 offset:20480
	v_mfma_f32_32x32x16_f16 v[50:65], v[200:203], v[204:207], v[50:65]
	ds_read_b128 v[168:171], v223 offset:16384
	v_mfma_f32_32x32x16_f16 v[18:33], v[200:203], v[208:211], v[18:33]
	ds_read_b128 v[172:175], v221
	v_mfma_f32_32x32x16_f16 v[34:49], v[212:215], v[204:207], v[34:49]
	ds_read_b128 v[176:179], v221 offset:4096
	v_mfma_f32_32x32x16_f16 v[2:17], v[212:215], v[208:211], v[2:17]
	ds_read_b128 v[180:183], v223 offset:20480
	s_waitcnt vmcnt(0) lgkmcnt(0)
	s_barrier
	v_mfma_f32_32x32x16_f16 v[50:65], v[152:155], v[156:159], v[50:65]
	ds_read_b128 v[184:187], v222 offset:49152
	v_mfma_f32_32x32x16_f16 v[18:33], v[152:155], v[160:163], v[18:33]
	ds_read_b128 v[188:191], v220 offset:32768
	v_mfma_f32_32x32x16_f16 v[34:49], v[164:167], v[156:159], v[34:49]
	ds_read_b128 v[192:195], v220 offset:36864
	v_mfma_f32_32x32x16_f16 v[2:17], v[164:167], v[160:163], v[2:17]
	ds_read_b128 v[196:199], v222 offset:53248
	v_mfma_f32_32x32x16_f16 v[50:65], v[168:171], v[172:175], v[50:65]
	ds_read_b128 v[200:203], v223 offset:49152
	v_mfma_f32_32x32x16_f16 v[18:33], v[168:171], v[176:179], v[18:33]
	ds_read_b128 v[204:207], v221 offset:32768
	v_mfma_f32_32x32x16_f16 v[34:49], v[180:183], v[172:175], v[34:49]
	ds_read_b128 v[208:211], v221 offset:36864
	v_mfma_f32_32x32x16_f16 v[2:17], v[180:183], v[176:179], v[2:17]
	ds_read_b128 v[212:215], v223 offset:53248
	s_waitcnt lgkmcnt(0)
	v_mfma_f32_32x32x16_f16 v[50:65], v[184:187], v[188:191], v[50:65]
	v_mfma_f32_32x32x16_f16 v[18:33], v[184:187], v[192:195], v[18:33]
	v_mfma_f32_32x32x16_f16 v[34:49], v[196:199], v[188:191], v[34:49]
	v_mfma_f32_32x32x16_f16 v[2:17], v[196:199], v[192:195], v[2:17]
	v_mfma_f32_32x32x16_f16 v[50:65], v[200:203], v[204:207], v[50:65]
	v_mfma_f32_32x32x16_f16 v[18:33], v[200:203], v[208:211], v[18:33]
	v_mfma_f32_32x32x16_f16 v[34:49], v[212:215], v[204:207], v[34:49]
	v_mfma_f32_32x32x16_f16 v[2:17], v[212:215], v[208:211], v[2:17]
	s_ashr_i32 s0, s23, 31
	s_xor_b32 s0, s0, s25
	s_abs_i32 s1, s23
	s_mul_hi_u32 s2, s1, s26
	s_mul_i32 s3, s2, s24
	s_sub_i32 s1, s1, s3
	s_add_i32 s3, s2, 1
	s_sub_i32 s14, s1, s24
	s_cmp_ge_u32 s1, s24
	s_cselect_b32 s2, s3, s2
	s_cselect_b32 s1, s14, s1
	s_add_i32 s3, s2, 1
	s_cmp_ge_u32 s1, s24
	s_cselect_b32 s1, s3, s2
	s_xor_b32 s1, s1, s0
	s_sub_i32 s0, s1, s0
	s_mul_i32 s1, s0, s21
	s_sub_i32 s15, s23, s1
	s_lshl_b32 s2, s15, 7
	s_lshl_b32 s14, s0, 7
	s_ashr_i32 s3, s2, 31
	s_waitcnt lgkmcnt(0)
	s_barrier
	s_nop 7
	ds_write_b128 v100, v[50:53]
	ds_write_b128 v101, v[54:57]
	ds_write_b128 v102, v[58:61]
	ds_write_b128 v103, v[62:65]
	ds_write_b128 v104, v[34:37]
	ds_write_b128 v105, v[38:41]
	ds_write_b128 v106, v[42:45]
	ds_write_b128 v107, v[46:49]
	ds_write_b128 v100, v[18:21] offset:16384
	ds_write_b128 v101, v[22:25] offset:16384
	ds_write_b128 v102, v[26:29] offset:16384
	ds_write_b128 v103, v[30:33] offset:16384
	ds_write_b128 v104, v[2:5] offset:16384
	ds_write_b128 v105, v[6:9] offset:16384
	ds_write_b128 v106, v[10:13] offset:16384
	ds_write_b128 v107, v[14:17] offset:16384
	v_or_b32_e32 v25, s14, v1
	v_lshl_add_u64 v[22:23], s[2:3], 1, v[70:71]
	s_waitcnt lgkmcnt(0)
	s_barrier
	v_mad_i64_i32 v[2:3], s[0:1], v25, s29, v[22:23]
	global_load_dwordx4 v[10:13], v[2:3], off
	v_lshl_add_u64 v[14:15], s[2:3], 2, v[68:69]
	global_load_dwordx4 v[6:9], v[14:15], off
	global_load_dwordx4 v[2:5], v[14:15], off offset:16
	v_add_u32_e32 v14, 0, v85
	v_add_u32_e32 v18, s28, v85
	ds_read_b128 v[14:17], v14
	ds_read_b128 v[26:29], v18
	v_or_b32_e32 v18, 32, v25
	v_mad_i64_i32 v[18:19], s[0:1], v18, s29, v[22:23]
	global_load_dwordx4 v[18:21], v[18:19], off
	s_waitcnt lgkmcnt(0)
	v_pk_add_f32 v[16:17], v[16:17], v[28:29]
	v_add_f32_e32 v35, v14, v26
	v_mov_b32_e32 v34, v27
	v_xor_b32_e32 v24, 8, v108
	s_waitcnt vmcnt(3)
	v_cvt_f32_f16_e32 v30, v11
	v_cvt_f32_f16_sdwa v31, v11 dst_sel:DWORD dst_unused:UNUSED_PAD src0_sel:WORD_1
	v_add_u32_e32 v11, 0, v86
	s_waitcnt vmcnt(2)
	v_pk_add_f32 v[16:17], v[8:9], v[16:17]
	ds_read_b128 v[26:29], v11
	v_add_u32_e32 v11, s28, v86
	v_pk_add_f32 v[36:37], v[16:17], v[30:31]
	ds_read_b128 v[30:33], v11
	v_cvt_f32_f16_e32 v38, v13
	v_cvt_f32_f16_sdwa v39, v13 dst_sel:DWORD dst_unused:UNUSED_PAD src0_sel:WORD_1
	s_waitcnt vmcnt(1)
	v_mov_b32_e32 v16, v2
	v_mov_b32_e32 v17, v3
	s_waitcnt lgkmcnt(0)
	v_pk_add_f32 v[28:29], v[28:29], v[32:33]
	v_cvt_f32_f16_e32 v32, v10
	v_pk_add_f32 v[28:29], v[4:5], v[28:29]
	v_pk_mov_b32 v[16:17], v[26:27], v[16:17] op_sel:[1,0]
	v_pk_add_f32 v[28:29], v[28:29], v[38:39]
	v_cvt_f32_f16_e32 v38, v12
	v_add_f32_e32 v26, v26, v30
	v_cvt_f32_f16_sdwa v33, v10 dst_sel:DWORD dst_unused:UNUSED_PAD src0_sel:WORD_1
	v_cvt_f32_f16_sdwa v30, v12 dst_sel:DWORD dst_unused:UNUSED_PAD src0_sel:WORD_1
	v_or_b32_e32 v12, 64, v25
	v_pk_mov_b32 v[14:15], v[14:15], v[6:7] op_sel:[1,0]
	v_mad_i64_i32 v[40:41], s[0:1], v12, s29, v[22:23]
	v_or_b32_e32 v12, 0x60, v25
	v_mov_b32_e32 v10, v31
	v_mov_b32_e32 v11, v26
	v_mad_i64_i32 v[42:43], s[0:1], v12, s29, v[22:23]
	v_pk_add_f32 v[44:45], v[14:15], v[34:35]
	v_mov_b32_e32 v12, v7
	v_mov_b32_e32 v13, v32
	v_pk_add_f32 v[10:11], v[16:17], v[10:11]
	v_pk_add_f32 v[46:47], v[12:13], v[44:45]
	v_mov_b32_e32 v22, v3
	v_mov_b32_e32 v23, v38
	v_pk_add_f32 v[48:49], v[22:23], v[10:11]
	v_mov_b32_e32 v10, v33
	v_mov_b32_e32 v11, v47
	v_pk_add_f32 v[50:51], v[46:47], v[10:11]
	global_load_dwordx4 v[14:17], v[40:41], off
	global_load_dwordx4 v[10:13], v[42:43], off
	v_mov_b32_e32 v31, v49
	v_pk_add_f32 v[40:41], v[48:49], v[30:31]
	v_pk_mov_b32 v[30:31], v[34:35], v[44:45] op_sel:[1,0]
	v_mov_b32_e32 v27, v44
	v_mov_b32_e32 v3, v7
	v_pk_add_f32 v[30:31], v[6:7], v[30:31]
	v_mov_b32_e32 v39, v33
	v_pk_add_f32 v[26:27], v[2:3], v[26:27]
	v_pk_add_f32 v[30:31], v[30:31], v[32:33]
	v_pk_add_f32 v[26:27], v[26:27], v[38:39]
	v_pk_mul_f32 v[32:33], v[46:47], v[46:47]
	v_pk_add_f32 v[34:35], v[30:31], v[26:27]
	v_pk_mul_f32 v[26:27], v[30:31], v[26:27]
	v_mov_b32_e32 v51, v33
	v_pk_mul_f32 v[32:33], v[48:49], v[48:49]
	v_mov_b32_e32 v35, v27
	v_pk_mul_f32 v[26:27], v[40:41], v[40:41]
	v_mov_b32_e32 v32, v40
	v_mov_b32_e32 v67, v26
	v_pk_add_f32 v[32:33], v[50:51], v[32:33]
	v_pk_add_f32 v[26:27], v[34:35], v[66:67]
	v_pk_mul_f32 v[30:31], v[36:37], v[36:37]
	v_pk_mul_f32 v[34:35], v[28:29], v[28:29]
	v_and_b32_e32 v23, 64, v108
	v_pk_add_f32 v[26:27], v[32:33], v[26:27]
	v_mov_b32_e32 v32, v36
	v_mov_b32_e32 v33, v30
	v_mov_b32_e32 v38, v28
	v_mov_b32_e32 v39, v34
	v_add_u32_e32 v23, 64, v23
	v_pk_add_f32 v[32:33], v[32:33], v[38:39]
	v_mov_b32_e32 v30, v37
	v_mov_b32_e32 v34, v29
	v_cmp_lt_i32_e64 s[0:1], v24, v23
	v_pk_add_f32 v[26:27], v[26:27], v[32:33]
	v_pk_add_f32 v[30:31], v[30:31], v[34:35]
	v_cndmask_b32_e64 v24, v108, v24, s[0:1]
	v_pk_add_f32 v[26:27], v[26:27], v[30:31]
	v_lshlrev_b32_e32 v30, 2, v24
	ds_bpermute_b32 v32, v30, v26
	ds_bpermute_b32 v33, v30, v27
	v_xor_b32_e32 v24, 4, v108
	v_cmp_lt_i32_e64 s[0:1], v24, v23
	v_cvt_pk_f16_f32 v39, v28, v29
	v_cvt_pk_f16_f32 v37, v36, v37
	v_cndmask_b32_e64 v24, v108, v24, s[0:1]
	s_waitcnt lgkmcnt(0)
	v_pk_add_f32 v[26:27], v[26:27], v[32:33]
	v_lshlrev_b32_e32 v31, 2, v24
	ds_bpermute_b32 v32, v31, v26
	ds_bpermute_b32 v33, v31, v27
	v_xor_b32_e32 v24, 2, v108
	v_cmp_lt_i32_e64 s[0:1], v24, v23
	v_cvt_pk_f16_f32 v36, v47, v50
	v_cvt_pk_f16_f32 v38, v49, v40
	v_cndmask_b32_e64 v24, v108, v24, s[0:1]
	s_waitcnt lgkmcnt(0)
	v_pk_add_f32 v[26:27], v[26:27], v[32:33]
	v_lshlrev_b32_e32 v33, 2, v24
	ds_bpermute_b32 v28, v33, v26
	ds_bpermute_b32 v29, v33, v27
	v_or_b32_e32 v32, s2, v78
	v_mul_lo_u32 v24, v25, s30
	v_add_lshl_u32 v24, v32, v24, 1
	buffer_store_dwordx4 v[36:39], v24, s[8:11], 0 offen sc1
	s_waitcnt lgkmcnt(0)
	v_pk_add_f32 v[26:27], v[26:27], v[28:29]
	v_xor_b32_e32 v28, 1, v108
	v_cmp_lt_i32_e64 s[0:1], v28, v23
	s_lshl_b32 s2, s15, 4
	v_mov_b32_e32 v24, v7
	v_cndmask_b32_e64 v23, v108, v28, s[0:1]
	v_lshlrev_b32_e32 v34, 2, v23
	ds_bpermute_b32 v28, v34, v26
	ds_bpermute_b32 v29, v34, v27
	s_and_saveexec_b64 s[0:1], vcc
	s_cbranch_execz .LBB9_5
	s_waitcnt lgkmcnt(0)
	v_pk_add_f32 v[64:65], v[26:27], v[28:29]
	v_lshl_add_u32 v23, v25, 6, s2
	v_mov_b32_e32 v67, v66
	s_mov_b32 s18, s10
	s_mov_b32 s19, s11
	buffer_store_dwordx4 v[64:67], v23, s[16:19], 0 offen sc1

	.amdhsa_kernel _Z6gemm_pILi2ELi32EEvPKDF16_S1_iiiiiiPKfS3_S3_PfPDF16_S4_S5_S4_
		.amdhsa_group_segment_fixed_size 0
		.amdhsa_private_segment_fixed_size 0
		.amdhsa_kernarg_size 360
		.amdhsa_user_sgpr_count 2
		.amdhsa_user_sgpr_dispatch_ptr 0
		.amdhsa_user_sgpr_queue_ptr 0
		.amdhsa_user_sgpr_kernarg_segment_ptr 1
		.amdhsa_user_sgpr_dispatch_id 0
		.amdhsa_user_sgpr_kernarg_preload_length 0
		.amdhsa_user_sgpr_kernarg_preload_offset 0
		.amdhsa_user_sgpr_private_segment_size 0
		.amdhsa_uses_dynamic_stack 0
		.amdhsa_enable_private_segment 0
		.amdhsa_system_sgpr_workgroup_id_x 1
		.amdhsa_system_sgpr_workgroup_id_y 0
		.amdhsa_system_sgpr_workgroup_id_z 0
		.amdhsa_system_sgpr_workgroup_info 0
		.amdhsa_system_vgpr_workitem_id 0
		.amdhsa_next_free_vgpr 224
		.amdhsa_next_free_sgpr 46
		.amdhsa_accum_offset 224
		.amdhsa_reserve_vcc 1
		.amdhsa_float_round_mode_32 0
		.amdhsa_float_round_mode_16_64 0
		.amdhsa_float_denorm_mode_32 3
		.amdhsa_float_denorm_mode_16_64 3
		.amdhsa_dx10_clamp 1
		.amdhsa_ieee_mode 1
		.amdhsa_fp16_overflow 0
		.amdhsa_tg_split 0
		.amdhsa_exception_fp_ieee_invalid_op 0
		.amdhsa_exception_fp_denorm_src 0
		.amdhsa_exception_fp_ieee_div_zero 0
		.amdhsa_exception_fp_ieee_overflow 0
		.amdhsa_exception_fp_ieee_underflow 0
		.amdhsa_exception_fp_ieee_inexact 0
		.amdhsa_exception_int_div_zero 0
	.end_amdhsa_kernel

.Lfunc_end9:
	.p2align	8
	.size	_Z6gemm_pILi2ELi32EEvPKDF16_S1_iiiiiiPKfS3_S3_PfPDF16_S4_S5_S4_, .Lfunc_end9-_Z6gemm_pILi2ELi32EEvPKDF16_S1_iiiiiiPKfS3_S3_PfPDF16_S4_S5_S4_
	.set _Z6gemm_pILi2ELi32EEvPKDF16_S1_iiiiiiPKfS3_S3_PfPDF16_S4_S5_S4_.num_vgpr, 148
	.set _Z6gemm_pILi2ELi32EEvPKDF16_S1_iiiiiiPKfS3_S3_PfPDF16_S4_S5_S4_.num_agpr, 0
	.set _Z6gemm_pILi2ELi32EEvPKDF16_S1_iiiiiiPKfS3_S3_PfPDF16_S4_S5_S4_.numbered_sgpr, 44
	.set _Z6gemm_pILi2ELi32EEvPKDF16_S1_iiiiiiPKfS3_S3_PfPDF16_S4_S5_S4_.num_named_barrier, 0
	.set _Z6gemm_pILi2ELi32EEvPKDF16_S1_iiiiiiPKfS3_S3_PfPDF16_S4_S5_S4_.private_seg_size, 0
	.set _Z6gemm_pILi2ELi32EEvPKDF16_S1_iiiiiiPKfS3_S3_PfPDF16_S4_S5_S4_.uses_vcc, 1
	.set _Z6gemm_pILi2ELi32EEvPKDF16_S1_iiiiiiPKfS3_S3_PfPDF16_S4_S5_S4_.uses_flat_scratch, 0
	.set _Z6gemm_pILi2ELi32EEvPKDF16_S1_iiiiiiPKfS3_S3_PfPDF16_S4_S5_S4_.has_dyn_sized_stack, 0
	.set _Z6gemm_pILi2ELi32EEvPKDF16_S1_iiiiiiPKfS3_S3_PfPDF16_S4_S5_S4_.has_recursion, 0
	.set _Z6gemm_pILi2ELi32EEvPKDF16_S1_iiiiiiPKfS3_S3_PfPDF16_S4_S5_S4_.has_indirect_call, 0

	.text
	.p2alignl 8, 3212836864
	.fill 256, 4, 3212836864

amdhsa.kernels:
  - .agpr_count:     0
    .args:
      - .actual_access:  read_only
        .address_space:  global
        .offset:         0
        .size:           8
        .value_kind:     global_buffer
      - .actual_access:  read_only
        .address_space:  global
        .offset:         8
        .size:           8
        .value_kind:     global_buffer
      - .actual_access:  read_only
        .address_space:  global
        .offset:         16
        .size:           8
        .value_kind:     global_buffer
      - .actual_access:  read_only
        .address_space:  global
        .offset:         24
        .size:           8
        .value_kind:     global_buffer
      - .actual_access:  write_only
        .address_space:  global
        .offset:         32
        .size:           8
        .value_kind:     global_buffer
      - .actual_access:  write_only
        .address_space:  global
        .offset:         40
        .size:           8
        .value_kind:     global_buffer
    .group_segment_fixed_size: 0
    .kernarg_segment_align: 8
    .kernarg_segment_size: 48
    .language:       OpenCL C
    .language_version:
      - 2
      - 0
    .max_flat_workgroup_size: 256
    .name:           _Z9fold_sumsPKfS0_S0_S0_PfS1_
    .private_segment_fixed_size: 0
    .sgpr_count:     15
    .sgpr_spill_count: 0
    .symbol:         _Z9fold_sumsPKfS0_S0_S0_PfS1_.kd
    .uniform_work_group_size: 1
    .uses_dynamic_stack: false
    .vgpr_count:     24
    .vgpr_spill_count: 0
    .wavefront_size: 64
  - .agpr_count:     0
    .args:
      - .offset:         0
        .size:           208
        .value_kind:     by_value
    .group_segment_fixed_size: 10496
    .kernarg_segment_align: 8
    .kernarg_segment_size: 208
    .language:       OpenCL C
    .language_version:
      - 2
      - 0
    .max_flat_workgroup_size: 256
    .name:           _Z15prologue_kernel12PrologueArgs
    .private_segment_fixed_size: 0
    .sgpr_count:     30
    .sgpr_spill_count: 0
    .symbol:         _Z15prologue_kernel12PrologueArgs.kd
    .uniform_work_group_size: 1
    .uses_dynamic_stack: false
    .vgpr_count:     35
    .vgpr_spill_count: 0
    .wavefront_size: 64
  - .agpr_count:     0
    .args:
      - .address_space:  global
        .offset:         0
        .size:           8
        .value_kind:     global_buffer
      - .address_space:  global
        .offset:         8
        .size:           8
        .value_kind:     global_buffer
      - .actual_access:  read_only
        .address_space:  global
        .offset:         16
        .size:           8
        .value_kind:     global_buffer
      - .actual_access:  read_only
        .address_space:  global
        .offset:         24
        .size:           8
        .value_kind:     global_buffer
      - .actual_access:  read_only
        .address_space:  global
        .offset:         32
        .size:           8
        .value_kind:     global_buffer
      - .actual_access:  write_only
        .address_space:  global
        .offset:         40
        .size:           8
        .value_kind:     global_buffer
      - .actual_access:  write_only
        .address_space:  global
        .offset:         48
        .size:           8
        .value_kind:     global_buffer
      - .offset:         56
        .size:           4
        .value_kind:     by_value
      - .offset:         60
        .size:           4
        .value_kind:     by_value
    .group_segment_fixed_size: 0
    .kernarg_segment_align: 8
    .kernarg_segment_size: 64
    .language:       OpenCL C
    .language_version:
      - 2
      - 0
    .max_flat_workgroup_size: 512
    .name:           _Z11attn_kernelPKDF16_PDF16_PKfS3_S3_PfS4_ii
    .private_segment_fixed_size: 0
    .sgpr_count:     34
    .sgpr_spill_count: 0
    .symbol:         _Z11attn_kernelPKDF16_PDF16_PKfS3_S3_PfS4_ii.kd
    .uniform_work_group_size: 1
    .uses_dynamic_stack: false
    .vgpr_count:     128
    .vgpr_spill_count: 0
    .wavefront_size: 64
  - .agpr_count:     0
    .args:
      - .actual_access:  read_only
        .address_space:  global
        .offset:         0
        .size:           8
        .value_kind:     global_buffer
      - .actual_access:  read_only
        .address_space:  global
        .offset:         8
        .size:           8
        .value_kind:     global_buffer
      - .actual_access:  write_only
        .address_space:  global
        .offset:         16
        .size:           8
        .value_kind:     global_buffer
    .group_segment_fixed_size: 64
    .kernarg_segment_align: 8
    .kernarg_segment_size: 24
    .language:       OpenCL C
    .language_version:
      - 2
      - 0
    .max_flat_workgroup_size: 1024
    .name:           _Z12loss_combinePKfS0_Pf
    .private_segment_fixed_size: 0
    .sgpr_count:     20
    .sgpr_spill_count: 0
    .symbol:         _Z12loss_combinePKfS0_Pf.kd
    .uniform_work_group_size: 1
    .uses_dynamic_stack: false
    .vgpr_count:     17
    .vgpr_spill_count: 0
    .wavefront_size: 64
  - .agpr_count:     0
    .args:
      - .actual_access:  read_only
        .address_space:  global
        .offset:         0
        .size:           8
        .value_kind:     global_buffer
      - .actual_access:  read_only
        .address_space:  global
        .offset:         8
        .size:           8
        .value_kind:     global_buffer
      - .actual_access:  write_only
        .address_space:  global
        .offset:         16
        .size:           8
        .value_kind:     global_buffer
    .group_segment_fixed_size: 16
    .kernarg_segment_align: 8
    .kernarg_segment_size: 24
    .language:       OpenCL C
    .language_version:
      - 2
      - 0
    .max_flat_workgroup_size: 256
    .name:           _Z9loss_rowsPKfPKiPf
    .private_segment_fixed_size: 0
    .sgpr_count:     18
    .sgpr_spill_count: 0
    .symbol:         _Z9loss_rowsPKfPKiPf.kd
    .uniform_work_group_size: 1
    .uses_dynamic_stack: false
    .vgpr_count:     28
    .vgpr_spill_count: 0
    .wavefront_size: 64
  - .agpr_count:     0
    .args:
      - .actual_access:  read_only
        .address_space:  global
        .offset:         0
        .size:           8
        .value_kind:     global_buffer
      - .actual_access:  write_only
        .address_space:  global
        .offset:         8
        .size:           8
        .value_kind:     global_buffer
    .group_segment_fixed_size: 16
    .kernarg_segment_align: 8
    .kernarg_segment_size: 16
    .language:       OpenCL C
    .language_version:
      - 2
      - 0
    .max_flat_workgroup_size: 256
    .name:           _Z10loss_finalPKfPf
    .private_segment_fixed_size: 0
    .sgpr_count:     10
    .sgpr_spill_count: 0
    .symbol:         _Z10loss_finalPKfPf.kd
    .uniform_work_group_size: 1
    .uses_dynamic_stack: false
    .vgpr_count:     6
    .vgpr_spill_count: 0
    .wavefront_size: 64
  - .agpr_count:     0
    .args:
      - .address_space:  global
        .offset:         0
        .size:           8
        .value_kind:     global_buffer
      - .address_space:  global
        .offset:         8
        .size:           8
        .value_kind:     global_buffer
      - .offset:         16
        .size:           4
        .value_kind:     by_value
      - .offset:         20
        .size:           4
        .value_kind:     by_value
      - .offset:         24
        .size:           4
        .value_kind:     by_value
      - .offset:         28
        .size:           4
        .value_kind:     by_value
      - .offset:         32
        .size:           4
        .value_kind:     by_value
      - .offset:         36
        .size:           4
        .value_kind:     by_value
      - .actual_access:  read_only
        .address_space:  global
        .offset:         40
        .size:           8
        .value_kind:     global_buffer
      - .actual_access:  read_only
        .address_space:  global
        .offset:         48
        .size:           8
        .value_kind:     global_buffer
      - .actual_access:  read_only
        .address_space:  global
        .offset:         56
        .size:           8
        .value_kind:     global_buffer
      - .actual_access:  read_only
        .address_space:  global
        .offset:         64
        .size:           8
        .value_kind:     global_buffer
      - .actual_access:  write_only
        .address_space:  global
        .offset:         72
        .size:           8
        .value_kind:     global_buffer
      - .offset:         80
        .size:           144
        .value_kind:     by_value
    .group_segment_fixed_size: 0
    .kernarg_segment_align: 8
    .kernarg_segment_size: 224
    .language:       OpenCL C
    .language_version:
      - 2
      - 0
    .max_flat_workgroup_size: 512
    .name:           _Z6gemm_qILi0ELi1EEvPKDF16_S1_iiiiiiPKfS3_S3_S3_PDF16_8ConvArgs
    .private_segment_fixed_size: 0
    .sgpr_count:     50
    .sgpr_spill_count: 0
    .symbol:         _Z6gemm_qILi0ELi1EEvPKDF16_S1_iiiiiiPKfS3_S3_S3_PDF16_8ConvArgs.kd
    .uniform_work_group_size: 1
    .uses_dynamic_stack: false
    .vgpr_count:     244
    .vgpr_spill_count: 0
    .wavefront_size: 64
  - .agpr_count:     0
    .args:
      - .actual_access:  read_only
        .address_space:  global
        .offset:         0
        .size:           8
        .value_kind:     global_buffer
      - .actual_access:  read_only
        .address_space:  global
        .offset:         8
        .size:           8
        .value_kind:     global_buffer
      - .offset:         16
        .size:           4
        .value_kind:     by_value
      - .offset:         20
        .size:           4
        .value_kind:     by_value
      - .offset:         24
        .size:           4
        .value_kind:     by_value
      - .offset:         28
        .size:           4
        .value_kind:     by_value
      - .offset:         32
        .size:           4
        .value_kind:     by_value
      - .offset:         36
        .size:           4
        .value_kind:     by_value
      - .actual_access:  read_only
        .address_space:  global
        .offset:         40
        .size:           8
        .value_kind:     global_buffer
      - .actual_access:  read_only
        .address_space:  global
        .offset:         48
        .size:           8
        .value_kind:     global_buffer
      - .actual_access:  read_only
        .address_space:  global
        .offset:         56
        .size:           8
        .value_kind:     global_buffer
      - .address_space:  global
        .offset:         64
        .size:           8
        .value_kind:     global_buffer
      - .address_space:  global
        .offset:         72
        .size:           8
        .value_kind:     global_buffer
      - .actual_access:  write_only
        .address_space:  global
        .offset:         80
        .size:           8
        .value_kind:     global_buffer
      - .actual_access:  read_only
        .address_space:  global
        .offset:         88
        .size:           8
        .value_kind:     global_buffer
      - .actual_access:  read_only
        .address_space:  global
        .offset:         96
        .size:           8
        .value_kind:     global_buffer
      - .offset:         104
        .size:           4
        .value_kind:     hidden_block_count_x
      - .offset:         108
        .size:           4
        .value_kind:     hidden_block_count_y
      - .offset:         112
        .size:           4
        .value_kind:     hidden_block_count_z
      - .offset:         116
        .size:           2
        .value_kind:     hidden_group_size_x
      - .offset:         118
        .size:           2
        .value_kind:     hidden_group_size_y
      - .offset:         120
        .size:           2
        .value_kind:     hidden_group_size_z
      - .offset:         122
        .size:           2
        .value_kind:     hidden_remainder_x
      - .offset:         124
        .size:           2
        .value_kind:     hidden_remainder_y
      - .offset:         126
        .size:           2
        .value_kind:     hidden_remainder_z
      - .offset:         144
        .size:           8
        .value_kind:     hidden_global_offset_x
      - .offset:         152
        .size:           8
        .value_kind:     hidden_global_offset_y
      - .offset:         160
        .size:           8
        .value_kind:     hidden_global_offset_z
      - .offset:         168
        .size:           2
        .value_kind:     hidden_grid_dims
      - .offset:         224
        .size:           4
        .value_kind:     hidden_dynamic_lds_size
    .group_segment_fixed_size: 0
    .kernarg_segment_align: 8
    .kernarg_segment_size: 360
    .language:       OpenCL C
    .language_version:
      - 2
      - 0
    .max_flat_workgroup_size: 512
    .name:           _Z6gemm_pILi2ELi8EEvPKDF16_S1_iiiiiiPKfS3_S3_PfPDF16_S4_S5_S4_
    .private_segment_fixed_size: 0
    .sgpr_count:     41
    .sgpr_spill_count: 0
    .symbol:         _Z6gemm_pILi2ELi8EEvPKDF16_S1_iiiiiiPKfS3_S3_PfPDF16_S4_S5_S4_.kd
    .uniform_work_group_size: 1
    .uses_dynamic_stack: false
    .vgpr_count:     150
    .vgpr_spill_count: 0
    .wavefront_size: 64
  - .agpr_count:     0
    .args:
      - .address_space:  global
        .offset:         0
        .size:           8
        .value_kind:     global_buffer
      - .address_space:  global
        .offset:         8
        .size:           8
        .value_kind:     global_buffer
      - .offset:         16
        .size:           4
        .value_kind:     by_value
      - .offset:         20
        .size:           4
        .value_kind:     by_value
      - .offset:         24
        .size:           4
        .value_kind:     by_value
      - .offset:         28
        .size:           4
        .value_kind:     by_value
      - .offset:         32
        .size:           4
        .value_kind:     by_value
      - .offset:         36
        .size:           4
        .value_kind:     by_value
      - .actual_access:  read_only
        .address_space:  global
        .offset:         40
        .size:           8
        .value_kind:     global_buffer
      - .actual_access:  read_only
        .address_space:  global
        .offset:         48
        .size:           8
        .value_kind:     global_buffer
      - .actual_access:  read_only
        .address_space:  global
        .offset:         56
        .size:           8
        .value_kind:     global_buffer
      - .actual_access:  read_only
        .address_space:  global
        .offset:         64
        .size:           8
        .value_kind:     global_buffer
      - .actual_access:  write_only
        .address_space:  global
        .offset:         72
        .size:           8
        .value_kind:     global_buffer
      - .offset:         80
        .size:           144
        .value_kind:     by_value
    .group_segment_fixed_size: 0
    .kernarg_segment_align: 8
    .kernarg_segment_size: 224
    .language:       OpenCL C
    .language_version:
      - 2
      - 0
    .max_flat_workgroup_size: 512
    .name:           _Z6gemm_qILi1ELi0EEvPKDF16_S1_iiiiiiPKfS3_S3_S3_PDF16_8ConvArgs
    .private_segment_fixed_size: 0
    .sgpr_count:     29
    .sgpr_spill_count: 0
    .symbol:         _Z6gemm_qILi1ELi0EEvPKDF16_S1_iiiiiiPKfS3_S3_S3_PDF16_8ConvArgs.kd
    .uniform_work_group_size: 1
    .uses_dynamic_stack: false
    .vgpr_count:     244
    .vgpr_spill_count: 0
    .wavefront_size: 64
  - .agpr_count:     0
    .args:
      - .actual_access:  read_only
        .address_space:  global
        .offset:         0
        .size:           8
        .value_kind:     global_buffer
      - .actual_access:  read_only
        .address_space:  global
        .offset:         8
        .size:           8
        .value_kind:     global_buffer
      - .offset:         16
        .size:           4
        .value_kind:     by_value
      - .offset:         20
        .size:           4
        .value_kind:     by_value
      - .offset:         24
        .size:           4
        .value_kind:     by_value
      - .offset:         28
        .size:           4
        .value_kind:     by_value
      - .offset:         32
        .size:           4
        .value_kind:     by_value
      - .offset:         36
        .size:           4
        .value_kind:     by_value
      - .actual_access:  read_only
        .address_space:  global
        .offset:         40
        .size:           8
        .value_kind:     global_buffer
      - .actual_access:  read_only
        .address_space:  global
        .offset:         48
        .size:           8
        .value_kind:     global_buffer
      - .actual_access:  read_only
        .address_space:  global
        .offset:         56
        .size:           8
        .value_kind:     global_buffer
      - .address_space:  global
        .offset:         64
        .size:           8
        .value_kind:     global_buffer
      - .address_space:  global
        .offset:         72
        .size:           8
        .value_kind:     global_buffer
      - .actual_access:  write_only
        .address_space:  global
        .offset:         80
        .size:           8
        .value_kind:     global_buffer
      - .actual_access:  read_only
        .address_space:  global
        .offset:         88
        .size:           8
        .value_kind:     global_buffer
      - .actual_access:  read_only
        .address_space:  global
        .offset:         96
        .size:           8
        .value_kind:     global_buffer
      - .offset:         104
        .size:           4
        .value_kind:     hidden_block_count_x
      - .offset:         108
        .size:           4
        .value_kind:     hidden_block_count_y
      - .offset:         112
        .size:           4
        .value_kind:     hidden_block_count_z
      - .offset:         116
        .size:           2
        .value_kind:     hidden_group_size_x
      - .offset:         118
        .size:           2
        .value_kind:     hidden_group_size_y
      - .offset:         120
        .size:           2
        .value_kind:     hidden_group_size_z
      - .offset:         122
        .size:           2
        .value_kind:     hidden_remainder_x
      - .offset:         124
        .size:           2
        .value_kind:     hidden_remainder_y
      - .offset:         126
        .size:           2
        .value_kind:     hidden_remainder_z
      - .offset:         144
        .size:           8
        .value_kind:     hidden_global_offset_x
      - .offset:         152
        .size:           8
        .value_kind:     hidden_global_offset_y
      - .offset:         160
        .size:           8
        .value_kind:     hidden_global_offset_z
      - .offset:         168
        .size:           2
        .value_kind:     hidden_grid_dims
      - .offset:         224
        .size:           4
        .value_kind:     hidden_dynamic_lds_size
    .group_segment_fixed_size: 0
    .kernarg_segment_align: 8
    .kernarg_segment_size: 360
    .language:       OpenCL C
    .language_version:
      - 2
      - 0
    .max_flat_workgroup_size: 512
    .name:           _Z6gemm_pILi2ELi32EEvPKDF16_S1_iiiiiiPKfS3_S3_PfPDF16_S4_S5_S4_
    .private_segment_fixed_size: 0
    .sgpr_count:     52
    .sgpr_spill_count: 0
    .symbol:         _Z6gemm_pILi2ELi32EEvPKDF16_S1_iiiiiiPKfS3_S3_PfPDF16_S4_S5_S4_.kd
    .uniform_work_group_size: 1
    .uses_dynamic_stack: false
    .vgpr_count:     224
    .vgpr_spill_count: 0
    .wavefront_size: 64
  - .agpr_count:     0
    .args:
      - .actual_access:  read_only
        .address_space:  global
        .offset:         0
        .size:           8
        .value_kind:     global_buffer
      - .actual_access:  read_only
        .address_space:  global
        .offset:         8
        .size:           8
        .value_kind:     global_buffer
      - .offset:         16
        .size:           4
        .value_kind:     by_value
      - .offset:         20
        .size:           4
        .value_kind:     by_value
      - .offset:         24
        .size:           4
        .value_kind:     by_value
      - .offset:         28
        .size:           4
        .value_kind:     by_value
      - .offset:         32
        .size:           4
        .value_kind:     by_value
      - .offset:         36
        .size:           4
        .value_kind:     by_value
      - .actual_access:  read_only
        .address_space:  global
        .offset:         40
        .size:           8
        .value_kind:     global_buffer
      - .actual_access:  read_only
        .address_space:  global
        .offset:         48
        .size:           8
        .value_kind:     global_buffer
      - .actual_access:  read_only
        .address_space:  global
        .offset:         56
        .size:           8
        .value_kind:     global_buffer
      - .address_space:  global
        .offset:         64
        .size:           8
        .value_kind:     global_buffer
      - .actual_access:  read_only
        .address_space:  global
        .offset:         72
        .size:           8
        .value_kind:     global_buffer
      - .actual_access:  write_only
        .address_space:  global
        .offset:         80
        .size:           8
        .value_kind:     global_buffer
      - .actual_access:  read_only
        .address_space:  global
        .offset:         88
        .size:           8
        .value_kind:     global_buffer
      - .actual_access:  write_only
        .address_space:  global
        .offset:         96
        .size:           8
        .value_kind:     global_buffer
      - .offset:         104
        .size:           4
        .value_kind:     hidden_block_count_x
      - .offset:         108
        .size:           4
        .value_kind:     hidden_block_count_y
      - .offset:         112
        .size:           4
        .value_kind:     hidden_block_count_z
      - .offset:         116
        .size:           2
        .value_kind:     hidden_group_size_x
      - .offset:         118
        .size:           2
        .value_kind:     hidden_group_size_y
      - .offset:         120
        .size:           2
        .value_kind:     hidden_group_size_z
      - .offset:         122
        .size:           2
        .value_kind:     hidden_remainder_x
      - .offset:         124
        .size:           2
        .value_kind:     hidden_remainder_y
      - .offset:         126
        .size:           2
        .value_kind:     hidden_remainder_z
      - .offset:         144
        .size:           8
        .value_kind:     hidden_global_offset_x
      - .offset:         152
        .size:           8
        .value_kind:     hidden_global_offset_y
      - .offset:         160
        .size:           8
        .value_kind:     hidden_global_offset_z
      - .offset:         168
        .size:           2
        .value_kind:     hidden_grid_dims
      - .offset:         224
        .size:           4
        .value_kind:     hidden_dynamic_lds_size
    .group_segment_fixed_size: 0
    .kernarg_segment_align: 8
    .kernarg_segment_size: 360
    .language:       OpenCL C
    .language_version:
      - 2
      - 0
    .max_flat_workgroup_size: 512
    .name:           _Z6gemm_pILi3ELi8EEvPKDF16_S1_iiiiiiPKfS3_S3_PfPDF16_S4_S5_S4_
    .private_segment_fixed_size: 0
    .sgpr_count:     46
    .sgpr_spill_count: 0
    .symbol:         _Z6gemm_pILi3ELi8EEvPKDF16_S1_iiiiiiPKfS3_S3_PfPDF16_S4_S5_S4_.kd
    .uniform_work_group_size: 1
    .uses_dynamic_stack: false
    .vgpr_count:     148
    .vgpr_spill_count: 0
    .wavefront_size: 64
